# speedup vs baseline: 1.2932x; 1.0129x over previous
.LBB0_65:
	s_or_b64 exec, exec, s[12:13]
	v_mov_b32_e32 v0, 0x20000
	s_waitcnt lgkmcnt(0)
	s_barrier
	ds_read_b96 v[186:188], v0
	v_lshlrev_b32_e32 v0, 10, v193
	s_load_dwordx4 s[12:15], s[0:1], 0x8
	v_and_b32_e32 v0, 0xc00, v0
	v_lshlrev_b32_e32 v1, 1, v193
	s_waitcnt lgkmcnt(0)
	v_readfirstlane_b32 s18, v188
	s_lshl_b32 s2, s18, 5
	v_add_u32_e32 v0, s2, v0
	v_bfe_u32 v109, v193, 4, 2
	v_and_or_b32 v0, v1, 24, v0
	s_lshr_b32 s3, s3, 6
	v_lshlrev_b32_e32 v217, 3, v109
	v_ashrrev_i32_e32 v1, 31, v0
	v_lshl_or_b32 v200, s3, 8, v217
	v_lshlrev_b64 v[4:5], 2, v[0:1]
	v_mov_b32_e32 v201, 0
	v_lshl_add_u64 v[6:7], s[14:15], 0, v[4:5]
	v_lshlrev_b64 v[0:1], 14, v[200:201]
	v_lshl_add_u64 v[0:1], v[6:7], 0, v[0:1]
	global_load_dwordx4 v[8:11], v[0:1], off offset:16
	global_load_dwordx4 v[12:15], v[0:1], off
	v_or_b32_e32 v0, 1, v200
	v_mov_b32_e32 v1, v201
	v_lshlrev_b64 v[0:1], 14, v[0:1]
	v_lshl_add_u64 v[0:1], v[6:7], 0, v[0:1]
	global_load_dwordx4 v[16:19], v[0:1], off offset:16
	global_load_dwordx4 v[20:23], v[0:1], off
	v_or_b32_e32 v0, 2, v200
	v_mov_b32_e32 v1, v201
	v_lshlrev_b64 v[0:1], 14, v[0:1]
	v_lshl_add_u64 v[0:1], v[6:7], 0, v[0:1]
	global_load_dwordx4 v[24:27], v[0:1], off offset:16
	global_load_dwordx4 v[28:31], v[0:1], off
	v_or_b32_e32 v0, 3, v200
	v_mov_b32_e32 v1, v201
	v_lshlrev_b64 v[0:1], 14, v[0:1]
	v_lshl_add_u64 v[0:1], v[6:7], 0, v[0:1]
	global_load_dwordx4 v[32:35], v[0:1], off offset:16
	global_load_dwordx4 v[36:39], v[0:1], off
	v_or_b32_e32 v0, 4, v200
	v_mov_b32_e32 v1, v201
	v_lshlrev_b64 v[0:1], 14, v[0:1]
	v_lshl_add_u64 v[0:1], v[6:7], 0, v[0:1]
	global_load_dwordx4 v[40:43], v[0:1], off offset:16
	global_load_dwordx4 v[44:47], v[0:1], off
	v_or_b32_e32 v0, 5, v200
	v_mov_b32_e32 v1, v201
	v_lshlrev_b64 v[0:1], 14, v[0:1]
	v_lshl_add_u64 v[0:1], v[6:7], 0, v[0:1]
	global_load_dwordx4 v[48:51], v[0:1], off offset:16
	global_load_dwordx4 v[52:55], v[0:1], off
	v_or_b32_e32 v0, 6, v200
	v_mov_b32_e32 v1, v201
	v_lshlrev_b64 v[0:1], 14, v[0:1]
	v_lshl_add_u64 v[0:1], v[6:7], 0, v[0:1]
	global_load_dwordx4 v[56:59], v[0:1], off offset:16
	global_load_dwordx4 v[60:63], v[0:1], off
	v_or_b32_e32 v0, 7, v200
	v_mov_b32_e32 v1, v201
	v_lshlrev_b64 v[0:1], 14, v[0:1]
	v_lshl_add_u64 v[0:1], v[6:7], 0, v[0:1]
	global_load_dwordx4 v[64:67], v[0:1], off offset:16
	global_load_dwordx4 v[68:71], v[0:1], off
	v_mov_b32_e32 v1, v201
	s_lshl_b32 s14, s3, 7
	v_and_b32_e32 v198, 63, v193
	v_lshlrev_b32_e32 v108, 4, v198
	v_lshl_or_b32 v95, s3, 15, v108
	s_lshl_b32 s0, s3, 11
	v_bfe_u32 v207, v193, 3, 3
	s_lshl_b32 s20, s3, 3
	v_or_b32_e32 v208, s20, v207
	v_readfirstlane_b32 s19, v187
	v_and_b32_e32 v150, 7, v193
	s_mov_b32 s15, 0
	v_or_b32_e32 v198, s0, v198
	s_mov_b32 s24, s15
	s_mov_b32 s25, s15
	s_mov_b32 s26, s15
	s_mov_b32 s27, s15
	v_and_b32_e32 v220, 15, v193
	s_lshl_b32 s22, s18, 2
	s_add_i32 s22, s22, s3
	s_lshl_b32 s21, s3, 12
	s_and_b32 s3, s22, 7
	s_ashr_i32 s23, s22, 3
	s_and_b32 s9, s9, 0xffff
	s_add_i32 s23, s23, 16
	v_mov_b32_e32 v202, v201
	v_mov_b32_e32 v203, v201
	s_mov_b32 s11, 0x20000
	s_mov_b32 s10, 0x40000
	s_waitcnt vmcnt(12)
	v_cvt_pk_f16_f32 v231, v12, v20
	v_accvgpr_write_b32 a0, v231
	s_waitcnt vmcnt(8)
	v_cvt_pk_f16_f32 v230, v28, v36
	v_accvgpr_write_b32 a1, v230
	s_waitcnt vmcnt(4)
	v_cvt_pk_f16_f32 v229, v44, v52
	v_accvgpr_write_b32 a2, v229
	s_waitcnt vmcnt(1)
	v_cvt_pk_f16_f32 v0, v56, v64
	v_accvgpr_write_b32 a131, v0
	v_cvt_pk_f16_f32 v0, v40, v48
	v_accvgpr_write_b32 a130, v0
	v_cvt_pk_f16_f32 v0, v24, v32
	v_accvgpr_write_b32 a129, v0
	v_cvt_pk_f16_f32 v0, v8, v16
	v_accvgpr_write_b32 a128, v0
	s_waitcnt vmcnt(0)
	v_cvt_pk_f16_f32 v0, v61, v69
	v_accvgpr_write_b32 a35, v0
	v_cvt_pk_f16_f32 v0, v45, v53
	v_accvgpr_write_b32 a34, v0
	v_cvt_pk_f16_f32 v0, v29, v37
	v_accvgpr_write_b32 a33, v0
	v_cvt_pk_f16_f32 v0, v13, v21
	v_accvgpr_write_b32 a32, v0
	v_cvt_pk_f16_f32 v0, v57, v65
	v_accvgpr_write_b32 a163, v0
	v_cvt_pk_f16_f32 v0, v41, v49
	v_accvgpr_write_b32 a162, v0
	v_cvt_pk_f16_f32 v0, v25, v33
	v_accvgpr_write_b32 a161, v0
	v_cvt_pk_f16_f32 v0, v9, v17
	v_accvgpr_write_b32 a160, v0
	v_cvt_pk_f16_f32 v0, v62, v70
	v_accvgpr_write_b32 a67, v0
	v_cvt_pk_f16_f32 v0, v46, v54
	v_accvgpr_write_b32 a66, v0
	v_cvt_pk_f16_f32 v0, v30, v38
	v_accvgpr_write_b32 a65, v0
	v_cvt_pk_f16_f32 v0, v14, v22
	v_accvgpr_write_b32 a64, v0
	v_cvt_pk_f16_f32 v0, v58, v66
	v_accvgpr_write_b32 a195, v0
	v_cvt_pk_f16_f32 v0, v42, v50
	v_accvgpr_write_b32 a194, v0
	v_cvt_pk_f16_f32 v0, v26, v34
	v_accvgpr_write_b32 a193, v0
	v_cvt_pk_f16_f32 v0, v10, v18
	v_accvgpr_write_b32 a192, v0
	v_cvt_pk_f16_f32 v0, v63, v71
	v_accvgpr_write_b32 a99, v0
	v_cvt_pk_f16_f32 v0, v47, v55
	v_accvgpr_write_b32 a98, v0
	v_cvt_pk_f16_f32 v0, v31, v39
	v_accvgpr_write_b32 a97, v0
	v_cvt_pk_f16_f32 v0, v15, v23
	v_accvgpr_write_b32 a96, v0
	v_cvt_pk_f16_f32 v0, v59, v67
	v_accvgpr_write_b32 a227, v0
	v_cvt_pk_f16_f32 v0, v43, v51
	v_accvgpr_write_b32 a226, v0
	v_cvt_pk_f16_f32 v0, v27, v35
	v_accvgpr_write_b32 a225, v0
	v_cvt_pk_f16_f32 v0, v11, v19
	v_accvgpr_write_b32 a224, v0
	v_or_b32_e32 v0, 32, v200
	v_lshlrev_b64 v[0:1], 14, v[0:1]
	v_lshl_add_u64 v[0:1], v[6:7], 0, v[0:1]
	global_load_dwordx4 v[8:11], v[0:1], off offset:16
	global_load_dwordx4 v[12:15], v[0:1], off
	v_or_b32_e32 v0, 33, v200
	v_mov_b32_e32 v1, v201
	v_lshlrev_b64 v[0:1], 14, v[0:1]
	v_lshl_add_u64 v[0:1], v[6:7], 0, v[0:1]
	global_load_dwordx4 v[16:19], v[0:1], off offset:16
	global_load_dwordx4 v[20:23], v[0:1], off
	v_or_b32_e32 v0, 34, v200
	v_mov_b32_e32 v1, v201
	v_lshlrev_b64 v[0:1], 14, v[0:1]
	v_lshl_add_u64 v[0:1], v[6:7], 0, v[0:1]
	global_load_dwordx4 v[24:27], v[0:1], off offset:16
	global_load_dwordx4 v[28:31], v[0:1], off
	v_or_b32_e32 v0, 35, v200
	v_mov_b32_e32 v1, v201
	v_lshlrev_b64 v[0:1], 14, v[0:1]
	v_lshl_add_u64 v[0:1], v[6:7], 0, v[0:1]
	global_load_dwordx4 v[32:35], v[0:1], off offset:16
	global_load_dwordx4 v[36:39], v[0:1], off
	v_or_b32_e32 v0, 36, v200
	v_mov_b32_e32 v1, v201
	v_lshlrev_b64 v[0:1], 14, v[0:1]
	v_lshl_add_u64 v[0:1], v[6:7], 0, v[0:1]
	global_load_dwordx4 v[40:43], v[0:1], off offset:16
	global_load_dwordx4 v[44:47], v[0:1], off
	v_or_b32_e32 v0, 37, v200
	v_mov_b32_e32 v1, v201
	v_lshlrev_b64 v[0:1], 14, v[0:1]
	v_lshl_add_u64 v[0:1], v[6:7], 0, v[0:1]
	global_load_dwordx4 v[48:51], v[0:1], off offset:16
	global_load_dwordx4 v[52:55], v[0:1], off
	v_or_b32_e32 v0, 38, v200
	v_mov_b32_e32 v1, v201
	v_lshlrev_b64 v[0:1], 14, v[0:1]
	v_lshl_add_u64 v[0:1], v[6:7], 0, v[0:1]
	v_cvt_pk_f16_f32 v228, v60, v68
	global_load_dwordx4 v[56:59], v[0:1], off offset:16
	global_load_dwordx4 v[60:63], v[0:1], off
	v_or_b32_e32 v0, 39, v200
	v_mov_b32_e32 v1, v201
	v_lshlrev_b64 v[0:1], 14, v[0:1]
	v_lshl_add_u64 v[0:1], v[6:7], 0, v[0:1]
	global_load_dwordx4 v[64:67], v[0:1], off offset:16
	global_load_dwordx4 v[68:71], v[0:1], off
	v_mov_b32_e32 v1, v201
	v_accvgpr_write_b32 a3, v228
	s_waitcnt vmcnt(12)
	v_cvt_pk_f16_f32 v206, v12, v20
	v_accvgpr_write_b32 a4, v206
	s_waitcnt vmcnt(8)
	v_cvt_pk_f16_f32 v197, v28, v36
	v_accvgpr_write_b32 a5, v197
	s_waitcnt vmcnt(4)
	v_cvt_pk_f16_f32 v199, v44, v52
	v_accvgpr_write_b32 a6, v199
	s_waitcnt vmcnt(1)
	v_cvt_pk_f16_f32 v0, v56, v64
	v_accvgpr_write_b32 a135, v0
	v_cvt_pk_f16_f32 v0, v40, v48
	v_accvgpr_write_b32 a134, v0
	v_cvt_pk_f16_f32 v0, v24, v32
	v_accvgpr_write_b32 a133, v0
	v_cvt_pk_f16_f32 v0, v8, v16
	v_accvgpr_write_b32 a132, v0
	s_waitcnt vmcnt(0)
	v_cvt_pk_f16_f32 v0, v61, v69
	v_accvgpr_write_b32 a39, v0
	v_cvt_pk_f16_f32 v0, v45, v53
	v_accvgpr_write_b32 a38, v0
	v_cvt_pk_f16_f32 v0, v29, v37
	v_accvgpr_write_b32 a37, v0
	v_cvt_pk_f16_f32 v0, v13, v21
	v_accvgpr_write_b32 a36, v0
	v_cvt_pk_f16_f32 v0, v57, v65
	v_accvgpr_write_b32 a167, v0
	v_cvt_pk_f16_f32 v0, v41, v49
	v_accvgpr_write_b32 a166, v0
	v_cvt_pk_f16_f32 v0, v25, v33
	v_accvgpr_write_b32 a165, v0
	v_cvt_pk_f16_f32 v0, v9, v17
	v_accvgpr_write_b32 a164, v0
	v_cvt_pk_f16_f32 v0, v62, v70
	v_accvgpr_write_b32 a71, v0
	v_cvt_pk_f16_f32 v0, v46, v54
	v_accvgpr_write_b32 a70, v0
	v_cvt_pk_f16_f32 v0, v30, v38
	v_accvgpr_write_b32 a69, v0
	v_cvt_pk_f16_f32 v0, v14, v22
	v_accvgpr_write_b32 a68, v0
	v_cvt_pk_f16_f32 v0, v58, v66
	v_accvgpr_write_b32 a199, v0
	v_cvt_pk_f16_f32 v0, v42, v50
	v_accvgpr_write_b32 a198, v0
	v_cvt_pk_f16_f32 v0, v26, v34
	v_accvgpr_write_b32 a197, v0
	v_cvt_pk_f16_f32 v0, v10, v18
	v_accvgpr_write_b32 a196, v0
	v_cvt_pk_f16_f32 v0, v63, v71
	v_accvgpr_write_b32 a103, v0
	v_cvt_pk_f16_f32 v0, v47, v55
	v_accvgpr_write_b32 a102, v0
	v_cvt_pk_f16_f32 v0, v31, v39
	v_accvgpr_write_b32 a101, v0
	v_cvt_pk_f16_f32 v0, v15, v23
	v_accvgpr_write_b32 a100, v0
	v_cvt_pk_f16_f32 v0, v59, v67
	v_accvgpr_write_b32 a231, v0
	v_cvt_pk_f16_f32 v0, v43, v51
	v_accvgpr_write_b32 a230, v0
	v_cvt_pk_f16_f32 v0, v27, v35
	v_accvgpr_write_b32 a229, v0
	v_cvt_pk_f16_f32 v0, v11, v19
	v_accvgpr_write_b32 a228, v0
	v_or_b32_e32 v0, 64, v200
	v_lshlrev_b64 v[0:1], 14, v[0:1]
	v_lshl_add_u64 v[0:1], v[6:7], 0, v[0:1]
	global_load_dwordx4 v[8:11], v[0:1], off offset:16
	global_load_dwordx4 v[12:15], v[0:1], off
	v_or_b32_e32 v0, 0x41, v200
	v_mov_b32_e32 v1, v201
	v_lshlrev_b64 v[0:1], 14, v[0:1]
	v_lshl_add_u64 v[0:1], v[6:7], 0, v[0:1]
	global_load_dwordx4 v[16:19], v[0:1], off offset:16
	global_load_dwordx4 v[20:23], v[0:1], off
	v_or_b32_e32 v0, 0x42, v200
	v_mov_b32_e32 v1, v201
	v_lshlrev_b64 v[0:1], 14, v[0:1]
	v_lshl_add_u64 v[0:1], v[6:7], 0, v[0:1]
	global_load_dwordx4 v[24:27], v[0:1], off offset:16
	global_load_dwordx4 v[28:31], v[0:1], off
	v_or_b32_e32 v0, 0x43, v200
	v_mov_b32_e32 v1, v201
	v_lshlrev_b64 v[0:1], 14, v[0:1]
	v_lshl_add_u64 v[0:1], v[6:7], 0, v[0:1]
	global_load_dwordx4 v[32:35], v[0:1], off offset:16
	global_load_dwordx4 v[36:39], v[0:1], off
	v_or_b32_e32 v0, 0x44, v200
	v_mov_b32_e32 v1, v201
	v_lshlrev_b64 v[0:1], 14, v[0:1]
	v_lshl_add_u64 v[0:1], v[6:7], 0, v[0:1]
	global_load_dwordx4 v[40:43], v[0:1], off offset:16
	global_load_dwordx4 v[44:47], v[0:1], off
	v_or_b32_e32 v0, 0x45, v200
	v_mov_b32_e32 v1, v201
	v_lshlrev_b64 v[0:1], 14, v[0:1]
	v_lshl_add_u64 v[0:1], v[6:7], 0, v[0:1]
	global_load_dwordx4 v[48:51], v[0:1], off offset:16
	global_load_dwordx4 v[52:55], v[0:1], off
	v_or_b32_e32 v0, 0x46, v200
	v_mov_b32_e32 v1, v201
	v_lshlrev_b64 v[0:1], 14, v[0:1]
	v_lshl_add_u64 v[0:1], v[6:7], 0, v[0:1]
	v_cvt_pk_f16_f32 v205, v60, v68
	global_load_dwordx4 v[56:59], v[0:1], off offset:16
	global_load_dwordx4 v[60:63], v[0:1], off
	v_or_b32_e32 v0, 0x47, v200
	v_mov_b32_e32 v1, v201
	v_lshlrev_b64 v[0:1], 14, v[0:1]
	v_lshl_add_u64 v[0:1], v[6:7], 0, v[0:1]
	global_load_dwordx4 v[64:67], v[0:1], off offset:16
	global_load_dwordx4 v[68:71], v[0:1], off
	v_mov_b32_e32 v1, v201
	v_accvgpr_write_b32 a7, v205
	s_waitcnt vmcnt(12)
	v_cvt_pk_f16_f32 v155, v12, v20
	v_accvgpr_write_b32 a8, v155
	s_waitcnt vmcnt(8)
	v_cvt_pk_f16_f32 v156, v28, v36
	v_accvgpr_write_b32 a9, v156
	s_waitcnt vmcnt(4)
	v_cvt_pk_f16_f32 v157, v44, v52
	v_accvgpr_write_b32 a10, v157
	s_waitcnt vmcnt(1)
	v_cvt_pk_f16_f32 v0, v56, v64
	v_accvgpr_write_b32 a139, v0
	v_cvt_pk_f16_f32 v0, v40, v48
	v_accvgpr_write_b32 a138, v0
	v_cvt_pk_f16_f32 v0, v24, v32
	v_accvgpr_write_b32 a137, v0
	v_cvt_pk_f16_f32 v0, v8, v16
	v_accvgpr_write_b32 a136, v0
	s_waitcnt vmcnt(0)
	v_cvt_pk_f16_f32 v0, v61, v69
	v_accvgpr_write_b32 a43, v0
	v_cvt_pk_f16_f32 v0, v45, v53
	v_accvgpr_write_b32 a42, v0
	v_cvt_pk_f16_f32 v0, v29, v37
	v_accvgpr_write_b32 a41, v0
	v_cvt_pk_f16_f32 v0, v13, v21
	v_accvgpr_write_b32 a40, v0
	v_cvt_pk_f16_f32 v0, v57, v65
	v_accvgpr_write_b32 a171, v0
	v_cvt_pk_f16_f32 v0, v41, v49
	v_accvgpr_write_b32 a170, v0
	v_cvt_pk_f16_f32 v0, v25, v33
	v_accvgpr_write_b32 a169, v0
	v_cvt_pk_f16_f32 v0, v9, v17
	v_accvgpr_write_b32 a168, v0
	v_cvt_pk_f16_f32 v0, v62, v70
	v_accvgpr_write_b32 a75, v0
	v_cvt_pk_f16_f32 v0, v46, v54
	v_accvgpr_write_b32 a74, v0
	v_cvt_pk_f16_f32 v0, v30, v38
	v_accvgpr_write_b32 a73, v0
	v_cvt_pk_f16_f32 v0, v14, v22
	v_accvgpr_write_b32 a72, v0
	v_cvt_pk_f16_f32 v0, v58, v66
	v_accvgpr_write_b32 a203, v0
	v_cvt_pk_f16_f32 v0, v42, v50
	v_accvgpr_write_b32 a202, v0
	v_cvt_pk_f16_f32 v0, v26, v34
	v_accvgpr_write_b32 a201, v0
	v_cvt_pk_f16_f32 v0, v10, v18
	v_accvgpr_write_b32 a200, v0
	v_cvt_pk_f16_f32 v0, v63, v71
	v_accvgpr_write_b32 a107, v0
	v_cvt_pk_f16_f32 v0, v47, v55
	v_accvgpr_write_b32 a106, v0
	v_cvt_pk_f16_f32 v0, v31, v39
	v_accvgpr_write_b32 a105, v0
	v_cvt_pk_f16_f32 v0, v15, v23
	v_accvgpr_write_b32 a104, v0
	v_cvt_pk_f16_f32 v0, v59, v67
	v_accvgpr_write_b32 a235, v0
	v_cvt_pk_f16_f32 v0, v43, v51
	v_accvgpr_write_b32 a234, v0
	v_cvt_pk_f16_f32 v0, v27, v35
	v_accvgpr_write_b32 a233, v0
	v_cvt_pk_f16_f32 v0, v11, v19
	v_accvgpr_write_b32 a232, v0
	v_or_b32_e32 v0, 0x60, v200
	v_lshlrev_b64 v[0:1], 14, v[0:1]
	v_lshl_add_u64 v[0:1], v[6:7], 0, v[0:1]
	global_load_dwordx4 v[8:11], v[0:1], off offset:16
	global_load_dwordx4 v[12:15], v[0:1], off
	v_or_b32_e32 v0, 0x61, v200
	v_mov_b32_e32 v1, v201
	v_lshlrev_b64 v[0:1], 14, v[0:1]
	v_lshl_add_u64 v[0:1], v[6:7], 0, v[0:1]
	global_load_dwordx4 v[16:19], v[0:1], off offset:16
	global_load_dwordx4 v[20:23], v[0:1], off
	v_or_b32_e32 v0, 0x62, v200
	v_mov_b32_e32 v1, v201
	v_lshlrev_b64 v[0:1], 14, v[0:1]
	v_lshl_add_u64 v[0:1], v[6:7], 0, v[0:1]
	global_load_dwordx4 v[24:27], v[0:1], off offset:16
	global_load_dwordx4 v[28:31], v[0:1], off
	v_or_b32_e32 v0, 0x63, v200
	v_mov_b32_e32 v1, v201
	v_lshlrev_b64 v[0:1], 14, v[0:1]
	v_lshl_add_u64 v[0:1], v[6:7], 0, v[0:1]
	global_load_dwordx4 v[32:35], v[0:1], off offset:16
	global_load_dwordx4 v[36:39], v[0:1], off
	v_or_b32_e32 v0, 0x64, v200
	v_mov_b32_e32 v1, v201
	v_lshlrev_b64 v[0:1], 14, v[0:1]
	v_lshl_add_u64 v[0:1], v[6:7], 0, v[0:1]
	global_load_dwordx4 v[40:43], v[0:1], off offset:16
	global_load_dwordx4 v[44:47], v[0:1], off
	v_or_b32_e32 v0, 0x65, v200
	v_mov_b32_e32 v1, v201
	v_lshlrev_b64 v[0:1], 14, v[0:1]
	v_lshl_add_u64 v[0:1], v[6:7], 0, v[0:1]
	global_load_dwordx4 v[48:51], v[0:1], off offset:16
	global_load_dwordx4 v[52:55], v[0:1], off
	v_or_b32_e32 v0, 0x66, v200
	v_mov_b32_e32 v1, v201
	v_lshlrev_b64 v[0:1], 14, v[0:1]
	v_lshl_add_u64 v[0:1], v[6:7], 0, v[0:1]
	v_cvt_pk_f16_f32 v158, v60, v68
	global_load_dwordx4 v[56:59], v[0:1], off offset:16
	global_load_dwordx4 v[60:63], v[0:1], off
	v_or_b32_e32 v0, 0x67, v200
	v_mov_b32_e32 v1, v201
	v_lshlrev_b64 v[0:1], 14, v[0:1]
	v_lshl_add_u64 v[0:1], v[6:7], 0, v[0:1]
	global_load_dwordx4 v[64:67], v[0:1], off offset:16
	global_load_dwordx4 v[68:71], v[0:1], off
	v_mov_b32_e32 v1, v201
	v_accvgpr_write_b32 a11, v158
	s_waitcnt vmcnt(12)
	v_cvt_pk_f16_f32 v122, v12, v20
	v_accvgpr_write_b32 a12, v122
	s_waitcnt vmcnt(8)
	v_cvt_pk_f16_f32 v123, v28, v36
	v_accvgpr_write_b32 a13, v123
	s_waitcnt vmcnt(4)
	v_cvt_pk_f16_f32 v124, v44, v52
	v_accvgpr_write_b32 a14, v124
	s_waitcnt vmcnt(1)
	v_cvt_pk_f16_f32 v0, v56, v64
	v_accvgpr_write_b32 a143, v0
	v_cvt_pk_f16_f32 v0, v40, v48
	v_accvgpr_write_b32 a142, v0
	v_cvt_pk_f16_f32 v0, v24, v32
	v_accvgpr_write_b32 a141, v0
	v_cvt_pk_f16_f32 v0, v8, v16
	v_accvgpr_write_b32 a140, v0
	s_waitcnt vmcnt(0)
	v_cvt_pk_f16_f32 v0, v61, v69
	v_accvgpr_write_b32 a47, v0
	v_cvt_pk_f16_f32 v0, v45, v53
	v_accvgpr_write_b32 a46, v0
	v_cvt_pk_f16_f32 v0, v29, v37
	v_accvgpr_write_b32 a45, v0
	v_cvt_pk_f16_f32 v0, v13, v21
	v_accvgpr_write_b32 a44, v0
	v_cvt_pk_f16_f32 v0, v57, v65
	v_accvgpr_write_b32 a175, v0
	v_cvt_pk_f16_f32 v0, v41, v49
	v_accvgpr_write_b32 a174, v0
	v_cvt_pk_f16_f32 v0, v25, v33
	v_accvgpr_write_b32 a173, v0
	v_cvt_pk_f16_f32 v0, v9, v17
	v_accvgpr_write_b32 a172, v0
	v_cvt_pk_f16_f32 v0, v62, v70
	v_accvgpr_write_b32 a79, v0
	v_cvt_pk_f16_f32 v0, v46, v54
	v_accvgpr_write_b32 a78, v0
	v_cvt_pk_f16_f32 v0, v30, v38
	v_accvgpr_write_b32 a77, v0
	v_cvt_pk_f16_f32 v0, v14, v22
	v_accvgpr_write_b32 a76, v0
	v_cvt_pk_f16_f32 v0, v58, v66
	v_accvgpr_write_b32 a207, v0
	v_cvt_pk_f16_f32 v0, v42, v50
	v_accvgpr_write_b32 a206, v0
	v_cvt_pk_f16_f32 v0, v26, v34
	v_accvgpr_write_b32 a205, v0
	v_cvt_pk_f16_f32 v0, v10, v18
	v_accvgpr_write_b32 a204, v0
	v_cvt_pk_f16_f32 v0, v63, v71
	v_accvgpr_write_b32 a111, v0
	v_cvt_pk_f16_f32 v0, v47, v55
	v_accvgpr_write_b32 a110, v0
	v_cvt_pk_f16_f32 v0, v31, v39
	v_accvgpr_write_b32 a109, v0
	v_cvt_pk_f16_f32 v0, v15, v23
	v_accvgpr_write_b32 a108, v0
	v_cvt_pk_f16_f32 v0, v59, v67
	v_accvgpr_write_b32 a239, v0
	v_cvt_pk_f16_f32 v0, v43, v51
	v_accvgpr_write_b32 a238, v0
	v_cvt_pk_f16_f32 v0, v27, v35
	v_accvgpr_write_b32 a237, v0
	v_cvt_pk_f16_f32 v0, v11, v19
	v_accvgpr_write_b32 a236, v0
	v_or_b32_e32 v0, 0x80, v200
	v_lshlrev_b64 v[0:1], 14, v[0:1]
	v_lshl_add_u64 v[0:1], v[6:7], 0, v[0:1]
	global_load_dwordx4 v[8:11], v[0:1], off offset:16
	global_load_dwordx4 v[12:15], v[0:1], off
	v_or_b32_e32 v0, 0x81, v200
	v_mov_b32_e32 v1, v201
	v_lshlrev_b64 v[0:1], 14, v[0:1]
	v_lshl_add_u64 v[0:1], v[6:7], 0, v[0:1]
	global_load_dwordx4 v[16:19], v[0:1], off offset:16
	global_load_dwordx4 v[20:23], v[0:1], off
	v_or_b32_e32 v0, 0x82, v200
	v_mov_b32_e32 v1, v201
	v_lshlrev_b64 v[0:1], 14, v[0:1]
	v_lshl_add_u64 v[0:1], v[6:7], 0, v[0:1]
	global_load_dwordx4 v[24:27], v[0:1], off offset:16
	global_load_dwordx4 v[28:31], v[0:1], off
	v_or_b32_e32 v0, 0x83, v200
	v_mov_b32_e32 v1, v201
	v_lshlrev_b64 v[0:1], 14, v[0:1]
	v_lshl_add_u64 v[0:1], v[6:7], 0, v[0:1]
	global_load_dwordx4 v[32:35], v[0:1], off offset:16
	global_load_dwordx4 v[36:39], v[0:1], off
	v_or_b32_e32 v0, 0x84, v200
	v_mov_b32_e32 v1, v201
	v_lshlrev_b64 v[0:1], 14, v[0:1]
	v_lshl_add_u64 v[0:1], v[6:7], 0, v[0:1]
	global_load_dwordx4 v[40:43], v[0:1], off offset:16
	global_load_dwordx4 v[44:47], v[0:1], off
	v_or_b32_e32 v0, 0x85, v200
	v_mov_b32_e32 v1, v201
	v_lshlrev_b64 v[0:1], 14, v[0:1]
	v_lshl_add_u64 v[0:1], v[6:7], 0, v[0:1]
	global_load_dwordx4 v[48:51], v[0:1], off offset:16
	global_load_dwordx4 v[52:55], v[0:1], off
	v_or_b32_e32 v0, 0x86, v200
	v_mov_b32_e32 v1, v201
	v_lshlrev_b64 v[0:1], 14, v[0:1]
	v_lshl_add_u64 v[0:1], v[6:7], 0, v[0:1]
	v_cvt_pk_f16_f32 v125, v60, v68
	global_load_dwordx4 v[56:59], v[0:1], off offset:16
	global_load_dwordx4 v[60:63], v[0:1], off
	v_or_b32_e32 v0, 0x87, v200
	v_mov_b32_e32 v1, v201
	v_lshlrev_b64 v[0:1], 14, v[0:1]
	v_lshl_add_u64 v[0:1], v[6:7], 0, v[0:1]
	global_load_dwordx4 v[64:67], v[0:1], off offset:16
	global_load_dwordx4 v[68:71], v[0:1], off
	v_mov_b32_e32 v1, v201
	v_accvgpr_write_b32 a15, v125
	s_waitcnt vmcnt(12)
	v_cvt_pk_f16_f32 v114, v12, v20
	v_cvt_pk_f16_f32 v245, v13, v21
	v_cvt_pk_f16_f32 v235, v14, v22
	v_cvt_pk_f16_f32 v227, v15, v23
	v_accvgpr_write_b32 a16, v114
	v_accvgpr_write_b32 a48, v245
	v_accvgpr_write_b32 a80, v235
	v_accvgpr_write_b32 a112, v227
	s_waitcnt vmcnt(8)
	v_cvt_pk_f16_f32 v115, v28, v36
	v_cvt_pk_f16_f32 v243, v29, v37
	v_cvt_pk_f16_f32 v234, v30, v38
	v_cvt_pk_f16_f32 v226, v31, v39
	v_accvgpr_write_b32 a17, v115
	v_accvgpr_write_b32 a49, v243
	v_accvgpr_write_b32 a81, v234
	v_accvgpr_write_b32 a113, v226
	s_waitcnt vmcnt(4)
	v_cvt_pk_f16_f32 v116, v44, v52
	v_cvt_pk_f16_f32 v241, v45, v53
	v_cvt_pk_f16_f32 v233, v46, v54
	v_cvt_pk_f16_f32 v225, v47, v55
	v_accvgpr_write_b32 a18, v116
	v_accvgpr_write_b32 a50, v241
	v_accvgpr_write_b32 a82, v233
	v_accvgpr_write_b32 a114, v225
	s_waitcnt vmcnt(1)
	v_cvt_pk_f16_f32 v0, v56, v64
	v_accvgpr_write_b32 a147, v0
	v_cvt_pk_f16_f32 v0, v40, v48
	v_accvgpr_write_b32 a146, v0
	v_cvt_pk_f16_f32 v0, v24, v32
	v_accvgpr_write_b32 a145, v0
	v_cvt_pk_f16_f32 v0, v8, v16
	v_accvgpr_write_b32 a144, v0
	v_cvt_pk_f16_f32 v0, v57, v65
	v_accvgpr_write_b32 a179, v0
	v_cvt_pk_f16_f32 v0, v41, v49
	v_accvgpr_write_b32 a178, v0
	v_cvt_pk_f16_f32 v0, v25, v33
	v_accvgpr_write_b32 a177, v0
	v_cvt_pk_f16_f32 v0, v9, v17
	v_accvgpr_write_b32 a176, v0
	v_cvt_pk_f16_f32 v0, v58, v66
	v_accvgpr_write_b32 a211, v0
	v_cvt_pk_f16_f32 v0, v42, v50
	v_accvgpr_write_b32 a210, v0
	v_cvt_pk_f16_f32 v0, v26, v34
	v_accvgpr_write_b32 a209, v0
	v_cvt_pk_f16_f32 v0, v10, v18
	v_accvgpr_write_b32 a208, v0
	s_waitcnt vmcnt(0)
	v_cvt_pk_f16_f32 v0, v63, v71
	v_accvgpr_write_b32 a115, v0
	v_cvt_pk_f16_f32 v0, v59, v67
	v_accvgpr_write_b32 a243, v0
	v_cvt_pk_f16_f32 v0, v43, v51
	v_accvgpr_write_b32 a242, v0
	v_cvt_pk_f16_f32 v0, v27, v35
	v_accvgpr_write_b32 a241, v0
	v_cvt_pk_f16_f32 v0, v11, v19
	v_accvgpr_write_b32 a240, v0
	v_or_b32_e32 v0, 0xa0, v200
	v_lshlrev_b64 v[0:1], 14, v[0:1]
	v_lshl_add_u64 v[0:1], v[6:7], 0, v[0:1]
	global_load_dwordx4 v[8:11], v[0:1], off offset:16
	global_load_dwordx4 v[12:15], v[0:1], off
	v_or_b32_e32 v0, 0xa1, v200
	v_mov_b32_e32 v1, v201
	v_lshlrev_b64 v[0:1], 14, v[0:1]
	v_lshl_add_u64 v[0:1], v[6:7], 0, v[0:1]
	global_load_dwordx4 v[16:19], v[0:1], off offset:16
	global_load_dwordx4 v[20:23], v[0:1], off
	v_or_b32_e32 v0, 0xa2, v200
	v_mov_b32_e32 v1, v201
	v_lshlrev_b64 v[0:1], 14, v[0:1]
	v_lshl_add_u64 v[0:1], v[6:7], 0, v[0:1]
	global_load_dwordx4 v[24:27], v[0:1], off offset:16
	global_load_dwordx4 v[28:31], v[0:1], off
	v_or_b32_e32 v0, 0xa3, v200
	v_mov_b32_e32 v1, v201
	v_lshlrev_b64 v[0:1], 14, v[0:1]
	v_lshl_add_u64 v[0:1], v[6:7], 0, v[0:1]
	global_load_dwordx4 v[32:35], v[0:1], off offset:16
	global_load_dwordx4 v[36:39], v[0:1], off
	v_or_b32_e32 v0, 0xa4, v200
	v_mov_b32_e32 v1, v201
	v_lshlrev_b64 v[0:1], 14, v[0:1]
	v_lshl_add_u64 v[0:1], v[6:7], 0, v[0:1]
	global_load_dwordx4 v[40:43], v[0:1], off offset:16
	global_load_dwordx4 v[44:47], v[0:1], off
	v_or_b32_e32 v0, 0xa5, v200
	v_mov_b32_e32 v1, v201
	v_lshlrev_b64 v[0:1], 14, v[0:1]
	v_lshl_add_u64 v[0:1], v[6:7], 0, v[0:1]
	global_load_dwordx4 v[48:51], v[0:1], off offset:16
	global_load_dwordx4 v[52:55], v[0:1], off
	v_or_b32_e32 v0, 0xa6, v200
	v_mov_b32_e32 v1, v201
	v_lshlrev_b64 v[0:1], 14, v[0:1]
	v_lshl_add_u64 v[0:1], v[6:7], 0, v[0:1]
	v_cvt_pk_f16_f32 v117, v60, v68
	v_cvt_pk_f16_f32 v240, v61, v69
	v_cvt_pk_f16_f32 v232, v62, v70
	global_load_dwordx4 v[56:59], v[0:1], off offset:16
	global_load_dwordx4 v[60:63], v[0:1], off
	v_or_b32_e32 v0, 0xa7, v200
	v_mov_b32_e32 v1, v201
	v_lshlrev_b64 v[0:1], 14, v[0:1]
	v_lshl_add_u64 v[0:1], v[6:7], 0, v[0:1]
	global_load_dwordx4 v[64:67], v[0:1], off offset:16
	global_load_dwordx4 v[68:71], v[0:1], off
	v_or_b32_e32 v0, 0xc0, v200
	v_mov_b32_e32 v1, v201
	v_lshlrev_b64 v[0:1], 14, v[0:1]
	v_lshl_add_u64 v[0:1], v[6:7], 0, v[0:1]
	v_accvgpr_write_b32 a19, v117
	v_accvgpr_write_b32 a51, v240
	v_accvgpr_write_b32 a83, v232
	s_waitcnt vmcnt(13)
	v_cvt_pk_f16_f32 v255, v8, v16
	s_waitcnt vmcnt(12)
	v_cvt_pk_f16_f32 v110, v12, v20
	v_cvt_pk_f16_f32 v204, v13, v21
	v_cvt_pk_f16_f32 v251, v9, v17
	v_cvt_pk_f16_f32 v196, v14, v22
	v_cvt_pk_f16_f32 v247, v10, v18
	v_cvt_pk_f16_f32 v212, v15, v23
	v_cvt_pk_f16_f32 v239, v11, v19
	global_load_dwordx4 v[8:11], v[0:1], off offset:16
	global_load_dwordx4 v[12:15], v[0:1], off
	v_or_b32_e32 v0, 0xc1, v200
	v_mov_b32_e32 v1, v201
	v_lshlrev_b64 v[0:1], 14, v[0:1]
	v_lshl_add_u64 v[0:1], v[6:7], 0, v[0:1]
	global_load_dwordx4 v[16:19], v[0:1], off offset:16
	global_load_dwordx4 v[20:23], v[0:1], off
	v_or_b32_e32 v0, 0xc2, v200
	v_mov_b32_e32 v1, v201
	v_lshlrev_b64 v[0:1], 14, v[0:1]
	v_lshl_add_u64 v[0:1], v[6:7], 0, v[0:1]
	s_waitcnt vmcnt(12)
	v_cvt_pk_f16_f32 v111, v28, v36
	v_cvt_pk_f16_f32 v254, v24, v32
	v_cvt_pk_f16_f32 v180, v29, v37
	v_cvt_pk_f16_f32 v250, v25, v33
	v_cvt_pk_f16_f32 v213, v30, v38
	v_cvt_pk_f16_f32 v246, v26, v34
	v_cvt_pk_f16_f32 v216, v31, v39
	v_cvt_pk_f16_f32 v238, v27, v35
	global_load_dwordx4 v[24:27], v[0:1], off offset:16
	global_load_dwordx4 v[28:31], v[0:1], off
	v_or_b32_e32 v0, 0xc3, v200
	v_mov_b32_e32 v1, v201
	v_lshlrev_b64 v[0:1], 14, v[0:1]
	v_lshl_add_u64 v[0:1], v[6:7], 0, v[0:1]
	global_load_dwordx4 v[32:35], v[0:1], off offset:16
	global_load_dwordx4 v[36:39], v[0:1], off
	v_or_b32_e32 v0, 0xc4, v200
	v_mov_b32_e32 v1, v201
	v_lshlrev_b64 v[0:1], 14, v[0:1]
	v_lshl_add_u64 v[0:1], v[6:7], 0, v[0:1]
	s_waitcnt vmcnt(12)
	v_cvt_pk_f16_f32 v112, v44, v52
	v_cvt_pk_f16_f32 v253, v40, v48
	v_cvt_pk_f16_f32 v181, v45, v53
	v_cvt_pk_f16_f32 v249, v41, v49
	v_cvt_pk_f16_f32 v219, v46, v54
	v_cvt_pk_f16_f32 v244, v42, v50
	v_cvt_pk_f16_f32 v218, v47, v55
	v_cvt_pk_f16_f32 v237, v43, v51
	global_load_dwordx4 v[40:43], v[0:1], off offset:16
	global_load_dwordx4 v[44:47], v[0:1], off
	v_or_b32_e32 v0, 0xc5, v200
	v_mov_b32_e32 v1, v201
	v_lshlrev_b64 v[0:1], 14, v[0:1]
	v_lshl_add_u64 v[0:1], v[6:7], 0, v[0:1]
	global_load_dwordx4 v[48:51], v[0:1], off offset:16
	global_load_dwordx4 v[52:55], v[0:1], off
	v_or_b32_e32 v0, 0xc6, v200
	v_mov_b32_e32 v1, v201
	v_lshlrev_b64 v[0:1], 14, v[0:1]
	v_lshl_add_u64 v[0:1], v[6:7], 0, v[0:1]
	s_waitcnt vmcnt(12)
	v_cvt_pk_f16_f32 v113, v60, v68
	v_cvt_pk_f16_f32 v252, v56, v64
	v_cvt_pk_f16_f32 v183, v61, v69
	v_cvt_pk_f16_f32 v248, v57, v65
	v_cvt_pk_f16_f32 v222, v62, v70
	v_cvt_pk_f16_f32 v242, v58, v66
	v_cvt_pk_f16_f32 v221, v63, v71
	v_cvt_pk_f16_f32 v236, v59, v67
	global_load_dwordx4 v[56:59], v[0:1], off offset:16
	global_load_dwordx4 v[60:63], v[0:1], off
	v_or_b32_e32 v0, 0xc7, v200
	v_mov_b32_e32 v1, v201
	v_lshlrev_b64 v[0:1], 14, v[0:1]
	v_lshl_add_u64 v[0:1], v[6:7], 0, v[0:1]
	global_load_dwordx4 v[64:67], v[0:1], off offset:16
	global_load_dwordx4 v[68:71], v[0:1], off
	v_or_b32_e32 v0, 0xe0, v200
	v_mov_b32_e32 v1, v201
	v_lshlrev_b64 v[0:1], 14, v[0:1]
	v_lshl_add_u64 v[0:1], v[6:7], 0, v[0:1]
	v_accvgpr_write_b32 a20, v110
	v_accvgpr_write_b32 a21, v111
	v_accvgpr_write_b32 a22, v112
	v_accvgpr_write_b32 a23, v113
	v_accvgpr_write_b32 a52, v204
	v_accvgpr_write_b32 a53, v180
	v_accvgpr_write_b32 a54, v181
	v_accvgpr_write_b32 a55, v183
	v_accvgpr_write_b32 a84, v196
	v_accvgpr_write_b32 a85, v213
	v_accvgpr_write_b32 a86, v219
	v_accvgpr_write_b32 a87, v222
	v_accvgpr_write_b32 a116, v212
	v_accvgpr_write_b32 a117, v216
	v_accvgpr_write_b32 a118, v218
	v_accvgpr_write_b32 a119, v221
	v_accvgpr_write_b32 a148, v255
	v_accvgpr_write_b32 a149, v254
	v_accvgpr_write_b32 a150, v253
	v_accvgpr_write_b32 a151, v252
	s_waitcnt vmcnt(13)
	v_cvt_pk_f16_f32 v167, v8, v16
	s_waitcnt vmcnt(12)
	v_cvt_pk_f16_f32 v190, v12, v20
	v_cvt_pk_f16_f32 v146, v13, v21
	v_cvt_pk_f16_f32 v171, v9, v17
	v_cvt_pk_f16_f32 v159, v14, v22
	v_cvt_pk_f16_f32 v176, v10, v18
	v_cvt_pk_f16_f32 v163, v15, v23
	v_cvt_pk_f16_f32 v189, v11, v19
	global_load_dwordx4 v[8:11], v[0:1], off offset:16
	global_load_dwordx4 v[12:15], v[0:1], off
	v_or_b32_e32 v0, 0xe1, v200
	v_mov_b32_e32 v1, v201
	v_lshlrev_b64 v[0:1], 14, v[0:1]
	v_lshl_add_u64 v[0:1], v[6:7], 0, v[0:1]
	global_load_dwordx4 v[16:19], v[0:1], off offset:16
	global_load_dwordx4 v[20:23], v[0:1], off
	v_or_b32_e32 v0, 0xe2, v200
	v_mov_b32_e32 v1, v201
	v_lshlrev_b64 v[0:1], 14, v[0:1]
	v_lshl_add_u64 v[0:1], v[6:7], 0, v[0:1]
	s_waitcnt vmcnt(13)
	v_cvt_pk_f16_f32 v168, v24, v32
	s_waitcnt vmcnt(12)
	v_cvt_pk_f16_f32 v224, v28, v36
	v_cvt_pk_f16_f32 v147, v29, v37
	v_cvt_pk_f16_f32 v172, v25, v33
	v_cvt_pk_f16_f32 v160, v30, v38
	v_cvt_pk_f16_f32 v177, v26, v34
	v_cvt_pk_f16_f32 v164, v31, v39
	v_cvt_pk_f16_f32 v191, v27, v35
	global_load_dwordx4 v[24:27], v[0:1], off offset:16
	global_load_dwordx4 v[28:31], v[0:1], off
	v_or_b32_e32 v0, 0xe3, v200
	v_mov_b32_e32 v1, v201
	v_lshlrev_b64 v[0:1], 14, v[0:1]
	v_lshl_add_u64 v[0:1], v[6:7], 0, v[0:1]
	global_load_dwordx4 v[32:35], v[0:1], off offset:16
	global_load_dwordx4 v[36:39], v[0:1], off
	v_or_b32_e32 v0, 0xe4, v200
	v_mov_b32_e32 v1, v201
	v_lshlrev_b64 v[0:1], 14, v[0:1]
	v_lshl_add_u64 v[0:1], v[6:7], 0, v[0:1]
	s_waitcnt vmcnt(13)
	v_cvt_pk_f16_f32 v169, v40, v48
	s_waitcnt vmcnt(12)
	v_cvt_pk_f16_f32 v223, v44, v52
	v_cvt_pk_f16_f32 v148, v45, v53
	v_cvt_pk_f16_f32 v174, v41, v49
	v_cvt_pk_f16_f32 v161, v46, v54
	v_cvt_pk_f16_f32 v178, v42, v50
	v_cvt_pk_f16_f32 v165, v47, v55
	v_cvt_pk_f16_f32 v192, v43, v51
	global_load_dwordx4 v[40:43], v[0:1], off offset:16
	global_load_dwordx4 v[44:47], v[0:1], off
	v_or_b32_e32 v0, 0xe5, v200
	v_mov_b32_e32 v1, v201
	v_lshlrev_b64 v[0:1], 14, v[0:1]
	v_lshl_add_u64 v[0:1], v[6:7], 0, v[0:1]
	global_load_dwordx4 v[48:51], v[0:1], off offset:16
	global_load_dwordx4 v[52:55], v[0:1], off
	v_or_b32_e32 v0, 0xe6, v200
	v_mov_b32_e32 v1, v201
	v_lshlrev_b64 v[0:1], 14, v[0:1]
	v_lshl_add_u64 v[0:1], v[6:7], 0, v[0:1]
	v_or_b32_e32 v200, 0xe7, v200
	s_waitcnt vmcnt(12)
	v_cvt_pk_f16_f32 v194, v60, v68
	v_cvt_pk_f16_f32 v170, v56, v64
	v_cvt_pk_f16_f32 v149, v61, v69
	v_cvt_pk_f16_f32 v175, v57, v65
	v_cvt_pk_f16_f32 v162, v62, v70
	v_cvt_pk_f16_f32 v179, v58, v66
	v_cvt_pk_f16_f32 v166, v63, v71
	v_cvt_pk_f16_f32 v195, v59, v67
	global_load_dwordx4 v[56:59], v[0:1], off offset:16
	global_load_dwordx4 v[60:63], v[0:1], off
	v_lshlrev_b64 v[0:1], 14, v[200:201]
	v_lshl_add_u64 v[0:1], v[6:7], 0, v[0:1]
	global_load_dwordx4 v[64:67], v[0:1], off offset:16
	global_load_dwordx4 v[68:71], v[0:1], off
	v_or_b32_e32 v200, s14, v217
	v_lshlrev_b64 v[0:1], 14, v[200:201]
	v_accvgpr_write_b32 a24, v190
	v_accvgpr_write_b32 a25, v224
	v_accvgpr_write_b32 a26, v223
	v_accvgpr_write_b32 a27, v194
	v_accvgpr_write_b32 a56, v146
	v_accvgpr_write_b32 a57, v147
	v_accvgpr_write_b32 a58, v148
	v_accvgpr_write_b32 a59, v149
	v_accvgpr_write_b32 a88, v159
	v_accvgpr_write_b32 a89, v160
	v_accvgpr_write_b32 a90, v161
	v_accvgpr_write_b32 a91, v162
	v_accvgpr_write_b32 a120, v163
	v_accvgpr_write_b32 a121, v164
	v_accvgpr_write_b32 a122, v165
	v_accvgpr_write_b32 a123, v166
	v_accvgpr_write_b32 a152, v167
	v_accvgpr_write_b32 a153, v168
	v_accvgpr_write_b32 a154, v169
	v_accvgpr_write_b32 a155, v170
	v_accvgpr_write_b32 a180, v251
	v_accvgpr_write_b32 a181, v250
	v_accvgpr_write_b32 a182, v249
	s_waitcnt vmcnt(13)
	v_cvt_pk_f16_f32 v134, v8, v16
	v_cvt_pk_f16_f32 v138, v9, v17
	v_cvt_pk_f16_f32 v142, v10, v18
	v_cvt_pk_f16_f32 v151, v11, v19
	s_waitcnt vmcnt(12)
	v_cvt_pk_f16_f32 v173, v12, v20
	v_cvt_pk_f16_f32 v118, v13, v21
	v_cvt_pk_f16_f32 v126, v14, v22
	v_cvt_pk_f16_f32 v130, v15, v23
	v_accvgpr_write_b32 a28, v173
	v_accvgpr_write_b32 a60, v118
	v_accvgpr_write_b32 a92, v126
	v_accvgpr_write_b32 a124, v130
	v_accvgpr_write_b32 a156, v134
	v_accvgpr_write_b32 a183, v248
	v_accvgpr_write_b32 a184, v171
	v_accvgpr_write_b32 a185, v172
	v_accvgpr_write_b32 a186, v174
	v_accvgpr_write_b32 a187, v175
	s_waitcnt vmcnt(9)
	v_cvt_pk_f16_f32 v135, v24, v32
	v_cvt_pk_f16_f32 v139, v25, v33
	v_cvt_pk_f16_f32 v143, v26, v34
	v_cvt_pk_f16_f32 v152, v27, v35
	s_waitcnt vmcnt(8)
	v_cvt_pk_f16_f32 v182, v28, v36
	v_cvt_pk_f16_f32 v119, v29, v37
	v_cvt_pk_f16_f32 v127, v30, v38
	v_cvt_pk_f16_f32 v131, v31, v39
	v_accvgpr_write_b32 a29, v182
	v_accvgpr_write_b32 a61, v119
	v_accvgpr_write_b32 a93, v127
	v_accvgpr_write_b32 a125, v131
	v_accvgpr_write_b32 a157, v135
	v_accvgpr_write_b32 a188, v138
	v_accvgpr_write_b32 a189, v139
	v_accvgpr_write_b32 a212, v247
	v_accvgpr_write_b32 a213, v246
	v_accvgpr_write_b32 a214, v244
	s_waitcnt vmcnt(5)
	v_cvt_pk_f16_f32 v136, v40, v48
	v_cvt_pk_f16_f32 v140, v41, v49
	v_cvt_pk_f16_f32 v144, v42, v50
	v_cvt_pk_f16_f32 v153, v43, v51
	s_waitcnt vmcnt(4)
	v_cvt_pk_f16_f32 v184, v44, v52
	v_cvt_pk_f16_f32 v120, v45, v53
	v_cvt_pk_f16_f32 v128, v46, v54
	v_cvt_pk_f16_f32 v132, v47, v55
	v_accvgpr_write_b32 a30, v184
	v_accvgpr_write_b32 a62, v120
	v_accvgpr_write_b32 a94, v128
	v_accvgpr_write_b32 a126, v132
	v_accvgpr_write_b32 a158, v136
	v_accvgpr_write_b32 a190, v140
	v_accvgpr_write_b32 a215, v242
	v_accvgpr_write_b32 a216, v176
	v_accvgpr_write_b32 a217, v177
	s_waitcnt vmcnt(1)
	v_cvt_pk_f16_f32 v137, v56, v64
	v_cvt_pk_f16_f32 v141, v57, v65
	v_lshl_add_u64 v[64:65], s[12:13], 0, v[4:5]
	v_lshl_add_u64 v[0:1], v[64:65], 0, v[0:1]
	global_load_dwordx4 v[4:7], v[0:1], off offset:16
	global_load_dwordx4 v[8:11], v[0:1], off
	v_or_b32_e32 v0, 1, v200
	v_mov_b32_e32 v1, v201
	v_lshlrev_b64 v[0:1], 14, v[0:1]
	v_lshl_add_u64 v[0:1], v[64:65], 0, v[0:1]
	global_load_dwordx4 v[12:15], v[0:1], off offset:16
	global_load_dwordx4 v[16:19], v[0:1], off
	v_or_b32_e32 v0, 2, v200
	v_mov_b32_e32 v1, v201
	v_lshlrev_b64 v[0:1], 14, v[0:1]
	v_lshl_add_u64 v[0:1], v[64:65], 0, v[0:1]
	global_load_dwordx4 v[20:23], v[0:1], off offset:16
	global_load_dwordx4 v[24:27], v[0:1], off
	v_or_b32_e32 v0, 3, v200
	v_mov_b32_e32 v1, v201
	v_lshlrev_b64 v[0:1], 14, v[0:1]
	v_lshl_add_u64 v[0:1], v[64:65], 0, v[0:1]
	global_load_dwordx4 v[28:31], v[0:1], off offset:16
	global_load_dwordx4 v[32:35], v[0:1], off
	v_or_b32_e32 v0, 4, v200
	v_mov_b32_e32 v1, v201
	v_lshlrev_b64 v[0:1], 14, v[0:1]
	v_lshl_add_u64 v[0:1], v[64:65], 0, v[0:1]
	global_load_dwordx4 v[36:39], v[0:1], off offset:16
	global_load_dwordx4 v[40:43], v[0:1], off
	v_or_b32_e32 v0, 5, v200
	v_mov_b32_e32 v1, v201
	v_lshlrev_b64 v[0:1], 14, v[0:1]
	v_lshl_add_u64 v[0:1], v[64:65], 0, v[0:1]
	global_load_dwordx4 v[44:47], v[0:1], off offset:16
	global_load_dwordx4 v[48:51], v[0:1], off
	v_or_b32_e32 v0, 6, v200
	v_mov_b32_e32 v1, v201
	v_lshlrev_b64 v[0:1], 14, v[0:1]
	v_lshl_add_u64 v[0:1], v[64:65], 0, v[0:1]
	v_cvt_pk_f16_f32 v145, v58, v66
	v_cvt_pk_f16_f32 v154, v59, v67
	global_load_dwordx4 v[52:55], v[0:1], off offset:16
	global_load_dwordx4 v[56:59], v[0:1], off
	v_or_b32_e32 v0, 7, v200
	v_mov_b32_e32 v1, v201
	v_lshlrev_b64 v[0:1], 14, v[0:1]
	v_lshl_add_u64 v[0:1], v[64:65], 0, v[0:1]
	s_waitcnt vmcnt(14)
	v_cvt_pk_f16_f32 v209, v60, v68
	v_cvt_pk_f16_f32 v121, v61, v69
	v_cvt_pk_f16_f32 v129, v62, v70
	v_cvt_pk_f16_f32 v133, v63, v71
	global_load_dwordx4 v[60:63], v[0:1], off offset:16
	global_load_dwordx4 v[66:69], v[0:1], off
	v_or_b32_e32 v0, 32, v200
	v_mov_b32_e32 v1, v201
	v_lshlrev_b64 v[0:1], 14, v[0:1]
	v_lshl_add_u64 v[0:1], v[64:65], 0, v[0:1]
	v_readfirstlane_b32 s12, v186
	s_lshl_b32 s13, s19, 3
	v_or_b32_e32 v214, s13, v150
	v_ashrrev_i32_e32 v215, 31, v214
	v_accvgpr_write_b32 a31, v209
	v_accvgpr_write_b32 a63, v121
	v_accvgpr_write_b32 a95, v129
	v_accvgpr_write_b32 a127, v133
	v_accvgpr_write_b32 a159, v137
	v_accvgpr_write_b32 a191, v141
	v_accvgpr_write_b32 a218, v178
	v_accvgpr_write_b32 a219, v179
	v_accvgpr_write_b32 a220, v142
	v_accvgpr_write_b32 a221, v143
	v_accvgpr_write_b32 a222, v144
	v_accvgpr_write_b32 a223, v145
	v_accvgpr_write_b32 a244, v239
	v_accvgpr_write_b32 a245, v238
	v_accvgpr_write_b32 a246, v237
	v_accvgpr_write_b32 a247, v236
	v_accvgpr_write_b32 a248, v189
	v_accvgpr_write_b32 a249, v191
	v_accvgpr_write_b32 a250, v192
	v_accvgpr_write_b32 a251, v195
	v_accvgpr_write_b32 a252, v151
	v_accvgpr_write_b32 a253, v152
	v_accvgpr_write_b32 a254, v153
	v_accvgpr_write_b32 a255, v154
	s_waitcnt vmcnt(13)
	v_cvt_pk_f16_f32 v74, v4, v12
	s_waitcnt vmcnt(12)
	v_cvt_pk_f16_f32 v70, v8, v16
	v_cvt_pk_f16_f32 v78, v9, v17
	v_cvt_pk_f16_f32 v82, v5, v13
	v_cvt_pk_f16_f32 v86, v10, v18
	v_cvt_pk_f16_f32 v2, v6, v14
	v_cvt_pk_f16_f32 v8, v7, v15
	s_waitcnt vmcnt(9)
	v_cvt_pk_f16_f32 v75, v20, v28
	s_waitcnt vmcnt(8)
	v_cvt_pk_f16_f32 v71, v24, v32
	v_cvt_pk_f16_f32 v79, v25, v33
	v_cvt_pk_f16_f32 v83, v21, v29
	v_cvt_pk_f16_f32 v87, v26, v34
	v_cvt_pk_f16_f32 v3, v22, v30
	v_cvt_pk_f16_f32 v27, v27, v35
	v_cvt_pk_f16_f32 v26, v11, v19
	v_cvt_pk_f16_f32 v9, v23, v31
	s_waitcnt vmcnt(5)
	v_cvt_pk_f16_f32 v76, v36, v44
	s_waitcnt vmcnt(4)
	v_cvt_pk_f16_f32 v72, v40, v48
	v_cvt_pk_f16_f32 v80, v41, v49
	v_cvt_pk_f16_f32 v84, v37, v45
	v_cvt_pk_f16_f32 v88, v42, v50
	v_cvt_pk_f16_f32 v4, v38, v46
	v_cvt_pk_f16_f32 v28, v43, v51
	v_cvt_pk_f16_f32 v10, v39, v47
	s_waitcnt vmcnt(1)
	v_cvt_pk_f16_f32 v77, v52, v60
	s_waitcnt vmcnt(0)
	v_cvt_pk_f16_f32 v73, v56, v66
	v_cvt_pk_f16_f32 v81, v57, v67
	v_cvt_pk_f16_f32 v85, v53, v61
	v_cvt_pk_f16_f32 v89, v58, v68
	v_cvt_pk_f16_f32 v5, v54, v62
	v_cvt_pk_f16_f32 v29, v59, v69
	v_cvt_pk_f16_f32 v11, v55, v63
	ds_write_b128 v95, v[70:73]
	ds_write_b128 v95, v[78:81] offset:1024
	ds_write_b128 v95, v[86:89] offset:2048
	ds_write_b128 v95, v[26:29] offset:3072
	ds_write_b128 v95, v[74:77] offset:4096
	ds_write_b128 v95, v[82:85] offset:5120
	ds_write_b128 v95, v[2:5] offset:6144
	ds_write_b128 v95, v[8:11] offset:7168
	global_load_dwordx4 v[4:7], v[0:1], off offset:16
	global_load_dwordx4 v[12:15], v[0:1], off
	v_or_b32_e32 v0, 33, v200
	v_mov_b32_e32 v1, v201
	v_lshlrev_b64 v[0:1], 14, v[0:1]
	v_lshl_add_u64 v[0:1], v[64:65], 0, v[0:1]
	global_load_dwordx4 v[8:11], v[0:1], off offset:16
	global_load_dwordx4 v[16:19], v[0:1], off
	v_or_b32_e32 v0, 34, v200
	v_mov_b32_e32 v1, v201
	v_lshlrev_b64 v[0:1], 14, v[0:1]
	v_lshl_add_u64 v[0:1], v[64:65], 0, v[0:1]
	global_load_dwordx4 v[20:23], v[0:1], off offset:16
	global_load_dwordx4 v[32:35], v[0:1], off
	v_or_b32_e32 v0, 35, v200
	v_mov_b32_e32 v1, v201
	v_lshlrev_b64 v[0:1], 14, v[0:1]
	v_lshl_add_u64 v[0:1], v[64:65], 0, v[0:1]
	global_load_dwordx4 v[24:27], v[0:1], off offset:16
	global_load_dwordx4 v[40:43], v[0:1], off
	v_or_b32_e32 v0, 36, v200
	v_mov_b32_e32 v1, v201
	v_lshlrev_b64 v[0:1], 14, v[0:1]
	v_lshl_add_u64 v[0:1], v[64:65], 0, v[0:1]
	global_load_dwordx4 v[28:31], v[0:1], off offset:16
	global_load_dwordx4 v[44:47], v[0:1], off
	v_or_b32_e32 v0, 37, v200
	v_mov_b32_e32 v1, v201
	v_lshlrev_b64 v[0:1], 14, v[0:1]
	v_lshl_add_u64 v[0:1], v[64:65], 0, v[0:1]
	global_load_dwordx4 v[36:39], v[0:1], off offset:16
	global_load_dwordx4 v[48:51], v[0:1], off
	v_or_b32_e32 v0, 38, v200
	v_mov_b32_e32 v1, v201
	v_lshlrev_b64 v[0:1], 14, v[0:1]
	v_lshl_add_u64 v[0:1], v[64:65], 0, v[0:1]
	global_load_dwordx4 v[52:55], v[0:1], off offset:16
	global_load_dwordx4 v[56:59], v[0:1], off
	v_or_b32_e32 v0, 39, v200
	v_mov_b32_e32 v1, v201
	v_lshlrev_b64 v[0:1], 14, v[0:1]
	v_lshl_add_u64 v[0:1], v[64:65], 0, v[0:1]
	global_load_dwordx4 v[60:63], v[0:1], off offset:16
	global_load_dwordx4 v[66:69], v[0:1], off
	v_or_b32_e32 v0, s0, v193
	v_lshlrev_b32_e32 v94, 4, v0
	v_or_b32_e32 v0, 0x3c00, v94
	v_mov_b32_e32 v1, v201
	v_bfe_u32 v193, v193, 3, 1
	v_cmp_gt_u32_e64 s[0:1], 8, v220
	s_waitcnt vmcnt(13)
	v_cvt_pk_f16_f32 v74, v4, v8
	s_waitcnt vmcnt(12)
	v_cvt_pk_f16_f32 v70, v12, v16
	v_cvt_pk_f16_f32 v78, v13, v17
	v_cvt_pk_f16_f32 v2, v14, v18
	v_cvt_pk_f16_f32 v12, v7, v11
	v_cvt_pk_f16_f32 v82, v5, v9
	v_cvt_pk_f16_f32 v86, v6, v10
	s_waitcnt vmcnt(9)
	v_cvt_pk_f16_f32 v13, v23, v27
	s_waitcnt vmcnt(8)
	v_cvt_pk_f16_f32 v71, v32, v40
	v_cvt_pk_f16_f32 v3, v34, v42
	v_cvt_pk_f16_f32 v34, v15, v19
	v_cvt_pk_f16_f32 v75, v20, v24
	v_cvt_pk_f16_f32 v79, v33, v41
	v_cvt_pk_f16_f32 v83, v21, v25
	v_cvt_pk_f16_f32 v87, v22, v26
	v_cvt_pk_f16_f32 v35, v35, v43
	s_waitcnt vmcnt(5)
	v_cvt_pk_f16_f32 v14, v31, v39
	s_waitcnt vmcnt(4)
	v_cvt_pk_f16_f32 v72, v44, v48
	v_cvt_pk_f16_f32 v76, v28, v36
	v_cvt_pk_f16_f32 v80, v45, v49
	v_cvt_pk_f16_f32 v84, v29, v37
	v_cvt_pk_f16_f32 v4, v46, v50
	v_cvt_pk_f16_f32 v88, v30, v38
	v_cvt_pk_f16_f32 v36, v47, v51
	s_waitcnt vmcnt(1)
	v_cvt_pk_f16_f32 v15, v55, v63
	s_waitcnt vmcnt(0)
	v_cvt_pk_f16_f32 v73, v56, v66
	v_cvt_pk_f16_f32 v77, v52, v60
	v_cvt_pk_f16_f32 v81, v57, v67
	v_cvt_pk_f16_f32 v85, v53, v61
	v_cvt_pk_f16_f32 v5, v58, v68
	v_cvt_pk_f16_f32 v89, v54, v62
	v_cvt_pk_f16_f32 v37, v59, v69
	ds_write_b128 v95, v[70:73] offset:8192
	ds_write_b128 v95, v[78:81] offset:9216
	ds_write_b128 v95, v[2:5] offset:10240
	ds_write_b128 v95, v[34:37] offset:11264
	ds_write_b128 v95, v[74:77] offset:12288
	ds_write_b128 v95, v[82:85] offset:13312
	ds_write_b128 v95, v[86:89] offset:14336
	ds_write_b128 v0, v[12:15]
	v_or_b32_e32 v0, 64, v200
	v_lshlrev_b64 v[0:1], 14, v[0:1]
	v_lshl_add_u64 v[0:1], v[64:65], 0, v[0:1]
	global_load_dwordx4 v[4:7], v[0:1], off offset:16
	global_load_dwordx4 v[8:11], v[0:1], off
	v_or_b32_e32 v0, 0x41, v200
	v_mov_b32_e32 v1, v201
	v_lshlrev_b64 v[0:1], 14, v[0:1]
	v_lshl_add_u64 v[0:1], v[64:65], 0, v[0:1]
	global_load_dwordx4 v[12:15], v[0:1], off offset:16
	global_load_dwordx4 v[16:19], v[0:1], off
	v_or_b32_e32 v0, 0x42, v200
	v_mov_b32_e32 v1, v201
	v_lshlrev_b64 v[0:1], 14, v[0:1]
	v_lshl_add_u64 v[0:1], v[64:65], 0, v[0:1]
	global_load_dwordx4 v[20:23], v[0:1], off offset:16
	global_load_dwordx4 v[28:31], v[0:1], off
	v_or_b32_e32 v0, 0x43, v200
	v_mov_b32_e32 v1, v201
	v_lshlrev_b64 v[0:1], 14, v[0:1]
	v_lshl_add_u64 v[0:1], v[64:65], 0, v[0:1]
	global_load_dwordx4 v[24:27], v[0:1], off offset:16
	global_load_dwordx4 v[32:35], v[0:1], off
	v_or_b32_e32 v0, 0x44, v200
	v_mov_b32_e32 v1, v201
	v_lshlrev_b64 v[0:1], 14, v[0:1]
	v_lshl_add_u64 v[0:1], v[64:65], 0, v[0:1]
	global_load_dwordx4 v[36:39], v[0:1], off offset:16
	global_load_dwordx4 v[40:43], v[0:1], off
	v_or_b32_e32 v0, 0x45, v200
	v_mov_b32_e32 v1, v201
	v_lshlrev_b64 v[0:1], 14, v[0:1]
	v_lshl_add_u64 v[0:1], v[64:65], 0, v[0:1]
	global_load_dwordx4 v[44:47], v[0:1], off offset:16
	global_load_dwordx4 v[48:51], v[0:1], off
	v_or_b32_e32 v0, 0x46, v200
	v_mov_b32_e32 v1, v201
	v_lshlrev_b64 v[0:1], 14, v[0:1]
	v_lshl_add_u64 v[0:1], v[64:65], 0, v[0:1]
	global_load_dwordx4 v[52:55], v[0:1], off offset:16
	global_load_dwordx4 v[56:59], v[0:1], off
	v_or_b32_e32 v0, 0x47, v200
	v_mov_b32_e32 v1, v201
	v_lshlrev_b64 v[0:1], 14, v[0:1]
	v_lshl_add_u64 v[0:1], v[64:65], 0, v[0:1]
	global_load_dwordx4 v[60:63], v[0:1], off offset:16
	global_load_dwordx4 v[66:69], v[0:1], off
	v_or_b32_e32 v0, 0x60, v200
	v_mov_b32_e32 v1, v201
	v_lshlrev_b64 v[0:1], 14, v[0:1]
	v_lshl_add_u64 v[0:1], v[64:65], 0, v[0:1]
	s_waitcnt vmcnt(13)
	v_cvt_pk_f16_f32 v74, v4, v12
	s_waitcnt vmcnt(12)
	v_cvt_pk_f16_f32 v70, v8, v16
	v_cvt_pk_f16_f32 v78, v9, v17
	v_cvt_pk_f16_f32 v82, v5, v13
	v_cvt_pk_f16_f32 v2, v10, v18
	v_cvt_pk_f16_f32 v86, v6, v14
	v_cvt_pk_f16_f32 v8, v7, v15
	s_waitcnt vmcnt(9)
	v_cvt_pk_f16_f32 v75, v20, v24
	s_waitcnt vmcnt(8)
	v_cvt_pk_f16_f32 v71, v28, v32
	v_cvt_pk_f16_f32 v79, v29, v33
	v_cvt_pk_f16_f32 v83, v21, v25
	v_cvt_pk_f16_f32 v3, v30, v34
	v_cvt_pk_f16_f32 v87, v22, v26
	v_cvt_pk_f16_f32 v31, v31, v35
	v_cvt_pk_f16_f32 v30, v11, v19
	v_cvt_pk_f16_f32 v9, v23, v27
	s_waitcnt vmcnt(5)
	v_cvt_pk_f16_f32 v76, v36, v44
	s_waitcnt vmcnt(4)
	v_cvt_pk_f16_f32 v72, v40, v48
	v_cvt_pk_f16_f32 v80, v41, v49
	v_cvt_pk_f16_f32 v84, v37, v45
	v_cvt_pk_f16_f32 v4, v42, v50
	v_cvt_pk_f16_f32 v88, v38, v46
	v_cvt_pk_f16_f32 v32, v43, v51
	v_cvt_pk_f16_f32 v10, v39, v47
	s_waitcnt vmcnt(1)
	v_cvt_pk_f16_f32 v77, v52, v60
	s_waitcnt vmcnt(0)
	v_cvt_pk_f16_f32 v73, v56, v66
	v_cvt_pk_f16_f32 v81, v57, v67
	v_cvt_pk_f16_f32 v85, v53, v61
	v_cvt_pk_f16_f32 v5, v58, v68
	v_cvt_pk_f16_f32 v89, v54, v62
	v_cvt_pk_f16_f32 v33, v59, v69
	v_cvt_pk_f16_f32 v11, v55, v63
	ds_write_b128 v95, v[70:73] offset:16384
	ds_write_b128 v95, v[78:81] offset:17408
	ds_write_b128 v95, v[2:5] offset:18432
	ds_write_b128 v95, v[30:33] offset:19456
	ds_write_b128 v95, v[74:77] offset:20480
	ds_write_b128 v95, v[82:85] offset:21504
	ds_write_b128 v95, v[86:89] offset:22528
	ds_write_b128 v95, v[8:11] offset:23552
	global_load_dwordx4 v[8:11], v[0:1], off offset:16
	global_load_dwordx4 v[40:43], v[0:1], off
	v_or_b32_e32 v0, 0x61, v200
	v_mov_b32_e32 v1, v201
	v_lshlrev_b64 v[0:1], 14, v[0:1]
	v_lshl_add_u64 v[0:1], v[64:65], 0, v[0:1]
	global_load_dwordx4 v[16:19], v[0:1], off offset:16
	global_load_dwordx4 v[48:51], v[0:1], off
	v_or_b32_e32 v0, 0x62, v200
	v_mov_b32_e32 v1, v201
	v_lshlrev_b64 v[0:1], 14, v[0:1]
	v_lshl_add_u64 v[0:1], v[64:65], 0, v[0:1]
	global_load_dwordx4 v[30:33], v[0:1], off offset:16
	global_load_dwordx4 v[56:59], v[0:1], off
	v_or_b32_e32 v0, 0x63, v200
	v_mov_b32_e32 v1, v201
	v_lshlrev_b64 v[0:1], 14, v[0:1]
	v_lshl_add_u64 v[0:1], v[64:65], 0, v[0:1]
	global_load_dwordx4 v[34:37], v[0:1], off offset:16
	global_load_dwordx4 v[60:63], v[0:1], off
	v_or_b32_e32 v0, 0x64, v200
	v_mov_b32_e32 v1, v201
	v_lshlrev_b64 v[0:1], 14, v[0:1]
	v_lshl_add_u64 v[0:1], v[64:65], 0, v[0:1]
	global_load_dwordx4 v[44:47], v[0:1], off offset:16
	global_load_dwordx4 v[72:75], v[0:1], off
	v_or_b32_e32 v0, 0x65, v200
	v_mov_b32_e32 v1, v201
	v_lshlrev_b64 v[0:1], 14, v[0:1]
	v_lshl_add_u64 v[0:1], v[64:65], 0, v[0:1]
	global_load_dwordx4 v[52:55], v[0:1], off offset:16
	global_load_dwordx4 v[80:83], v[0:1], off
	v_or_b32_e32 v0, 0x66, v200
	v_mov_b32_e32 v1, v201
	v_lshlrev_b64 v[0:1], 14, v[0:1]
	v_lshl_add_u64 v[0:1], v[64:65], 0, v[0:1]
	v_or_b32_e32 v200, 0x67, v200
	global_load_dwordx4 v[68:71], v[0:1], off offset:16
	global_load_dwordx4 v[84:87], v[0:1], off
	v_lshlrev_b64 v[0:1], 14, v[200:201]
	v_lshl_add_u64 v[0:1], v[64:65], 0, v[0:1]
	global_load_dwordx4 v[76:79], v[0:1], off offset:16
	s_nop 0
	global_load_dwordx4 v[0:3], v[0:1], off
	v_lshlrev_b32_e32 v200, 5, v109
	s_waitcnt vmcnt(13)
	v_cvt_pk_f16_f32 v4, v8, v16
	s_waitcnt vmcnt(12)
	v_cvt_pk_f16_f32 v64, v40, v48
	v_cvt_pk_f16_f32 v20, v41, v49
	v_cvt_pk_f16_f32 v12, v9, v17
	v_cvt_pk_f16_f32 v28, v42, v50
	v_cvt_pk_f16_f32 v24, v10, v18
	v_cvt_pk_f16_f32 v38, v43, v51
	s_waitcnt vmcnt(9)
	v_cvt_pk_f16_f32 v5, v30, v34
	s_waitcnt vmcnt(8)
	v_cvt_pk_f16_f32 v65, v56, v60
	v_cvt_pk_f16_f32 v13, v31, v35
	v_cvt_pk_f16_f32 v25, v32, v36
	v_cvt_pk_f16_f32 v33, v33, v37
	v_cvt_pk_f16_f32 v32, v11, v19
	v_cvt_pk_f16_f32 v21, v57, v61
	v_cvt_pk_f16_f32 v29, v58, v62
	v_cvt_pk_f16_f32 v39, v59, v63
	s_waitcnt vmcnt(5)
	v_cvt_pk_f16_f32 v26, v46, v54
	v_add_u32_e32 v54, s2, v208
	s_waitcnt vmcnt(4)
	v_cvt_pk_f16_f32 v66, v72, v80
	v_cvt_pk_f16_f32 v34, v47, v55
	v_ashrrev_i32_e32 v55, 31, v54
	v_cvt_pk_f16_f32 v6, v44, v52
	v_cvt_pk_f16_f32 v22, v73, v81
	v_cvt_pk_f16_f32 v14, v45, v53
	v_cvt_pk_f16_f32 v30, v74, v82
	s_waitcnt vmcnt(1)
	v_cvt_pk_f16_f32 v35, v71, v79
	s_waitcnt vmcnt(0)
	v_cvt_pk_f16_f32 v67, v84, v0
	v_or_b32_e32 v0, 0x7c00, v94
	v_cvt_pk_f16_f32 v7, v68, v76
	v_cvt_pk_f16_f32 v23, v85, v1
	v_cvt_pk_f16_f32 v15, v69, v77
	v_cvt_pk_f16_f32 v31, v86, v2
	v_cvt_pk_f16_f32 v27, v70, v78
	v_cvt_pk_f16_f32 v41, v87, v3
	v_cvt_pk_f16_f32 v40, v75, v83
	ds_write_b128 v95, v[64:67] offset:24576
	ds_write_b128 v95, v[20:23] offset:25600
	ds_write_b128 v95, v[28:31] offset:26624
	ds_write_b128 v95, v[38:41] offset:27648
	ds_write_b128 v95, v[4:7] offset:28672
	ds_write_b128 v95, v[12:15] offset:29696
	ds_write_b128 v95, v[24:27] offset:30720
	ds_write_b128 v0, v[32:35]
	v_lshl_add_u64 v[0:1], v[54:55], 2, s[4:5]
	global_load_dword v185, v[0:1], off
	v_add_u32_e32 v0, 0x400, v54
	v_ashrrev_i32_e32 v1, 31, v0
	v_lshl_add_u64 v[0:1], v[0:1], 2, s[4:5]
	global_load_dword v186, v[0:1], off
	v_add_u32_e32 v0, 0x800, v54
	v_ashrrev_i32_e32 v1, 31, v0
	v_lshl_add_u64 v[0:1], v[0:1], 2, s[4:5]
	global_load_dword v187, v[0:1], off
	v_add_u32_e32 v0, 0xc00, v54
	v_ashrrev_i32_e32 v1, 31, v0
	v_lshl_add_u64 v[0:1], v[0:1], 2, s[4:5]
	global_load_dword v188, v[0:1], off
	v_lshlrev_b64 v[0:1], 20, v[214:215]
	v_lshl_add_u64 v[0:1], s[16:17], 0, v[0:1]
	v_lshl_add_u64 v[0:1], s[14:15], 2, v[0:1]
	v_lshl_add_u64 v[210:211], v[0:1], 0, v[200:201]
	global_load_dwordx4 v[4:7], v[210:211], off offset:256
	global_load_dwordx4 v[8:11], v[210:211], off offset:272
	global_load_dwordx4 v[14:17], v[210:211], off offset:384
	global_load_dwordx4 v[18:21], v[210:211], off offset:400
	v_lshlrev_b32_e32 v0, 4, v198
	s_waitcnt lgkmcnt(0)
	s_barrier
	ds_read_b128 v[96:99], v0 offset:23552
	ds_read_b128 v[92:95], v0 offset:22528
	ds_read_b128 v[88:91], v0 offset:21504
	ds_read_b128 v[60:63], v0 offset:20480
	ds_read_b128 v[64:67], v0 offset:19456
	ds_read_b128 v[68:71], v0 offset:18432
	ds_read_b128 v[72:75], v0 offset:17408
	ds_read_b128 v[76:79], v0 offset:16384
	v_mov_b64_e32 v[44:45], s[26:27]
	v_mov_b64_e32 v[40:41], s[26:27]
	v_mov_b64_e32 v[22:23], s[24:25]
	v_mov_b64_e32 v[28:29], s[26:27]
	v_mov_b64_e32 v[32:33], s[26:27]
	v_mov_b64_e32 v[36:37], s[26:27]
	v_mov_b64_e32 v[42:43], s[24:25]
	v_mov_b64_e32 v[38:39], s[24:25]
	v_mov_b64_e32 v[24:25], s[26:27]
	v_mov_b64_e32 v[26:27], s[24:25]
	v_mov_b64_e32 v[30:31], s[24:25]
	v_mov_b64_e32 v[34:35], s[24:25]
	s_or_b32 s4, s3, s13
	s_ashr_i32 s5, s4, 31
	s_lshl_b64 s[4:5], s[4:5], 20
	s_add_u32 s4, s16, s4
	s_addc_u32 s5, s17, s5
	s_cmp_lg_u32 s12, 0
	v_mov_b32_e32 v200, v201
	s_waitcnt vmcnt(3)
	v_cvt_pk_f16_f32 v101, v6, v7
	s_waitcnt vmcnt(2)
	v_cvt_pk_f16_f32 v103, v10, v11
	v_cvt_pk_f16_f32 v102, v8, v9
	v_cvt_pk_f16_f32 v100, v4, v5
	ds_read_b128 v[80:83], v0 offset:31744
	ds_read_b128 v[84:87], v0 offset:30720
	ds_read_b128 v[56:59], v0 offset:29696
	ds_read_b128 v[50:53], v0 offset:28672
	ds_read_b128 v[46:49], v0 offset:27648
	ds_read_b128 v[8:11], v0 offset:26624
	ds_read_b128 v[4:7], v0 offset:25600
	ds_read_b128 v[0:3], v0 offset:24576
	s_waitcnt vmcnt(0)
	v_cvt_pk_f16_f32 v107, v20, v21
	v_cvt_pk_f16_f32 v106, v18, v19
	v_cvt_pk_f16_f32 v105, v16, v17
	v_cvt_pk_f16_f32 v104, v14, v15
	v_mov_b64_e32 v[14:15], s[24:25]
	v_mov_b64_e32 v[18:19], s[24:25]
	v_mov_b64_e32 v[16:17], s[26:27]
	v_mov_b64_e32 v[20:21], s[26:27]
	s_waitcnt lgkmcnt(8)
	s_nop 1
	v_mfma_f32_16x16x32_f16 v[42:45], v[76:79], v[100:103], v[42:45]
	v_mfma_f32_16x16x32_f16 v[38:41], v[72:75], v[100:103], v[38:41]
	v_mfma_f32_16x16x32_f16 v[14:17], v[68:71], v[100:103], v[14:17]
	v_mfma_f32_16x16x32_f16 v[18:21], v[64:67], v[100:103], v[18:21]
	v_mfma_f32_16x16x32_f16 v[22:25], v[60:63], v[100:103], v[22:25]
	v_mfma_f32_16x16x32_f16 v[26:29], v[88:91], v[100:103], v[26:29]
	v_mfma_f32_16x16x32_f16 v[30:33], v[92:95], v[100:103], v[30:33]
	v_mfma_f32_16x16x32_f16 v[34:37], v[96:99], v[100:103], v[34:37]
	v_lshlrev_b32_e32 v103, 4, v150
	s_waitcnt lgkmcnt(0)
	s_nop 1
	v_mfma_f32_16x16x32_f16 v[42:45], v[0:3], v[104:107], v[42:45]
	v_mfma_f32_16x16x32_f16 v[38:41], v[4:7], v[104:107], v[38:41]
	v_mfma_f32_16x16x32_f16 v[14:17], v[8:11], v[104:107], v[14:17]
	v_mfma_f32_16x16x32_f16 v[18:21], v[46:49], v[104:107], v[18:21]
	v_mfma_f32_16x16x32_f16 v[22:25], v[50:53], v[104:107], v[22:25]
	v_mfma_f32_16x16x32_f16 v[26:29], v[56:59], v[104:107], v[26:29]
	v_mfma_f32_16x16x32_f16 v[30:33], v[84:87], v[104:107], v[30:33]
	v_mfma_f32_16x16x32_f16 v[34:37], v[80:83], v[104:107], v[34:37]
	v_lshlrev_b32_e32 v0, 11, v193
	v_mov_b32_e32 v1, v201
	s_nop 15
	s_nop 7
	v_lshl_add_u64 v[0:1], v[210:211], 0, v[0:1]
	v_cndmask_b32_e64 v6, 0, v42, s[0:1]
	v_cndmask_b32_e64 v7, 0, v43, s[0:1]
	v_cndmask_b32_e64 v8, 0, v44, s[0:1]
	v_cndmask_b32_e64 v9, 0, v45, s[0:1]
	v_cndmask_b32_e64 v10, 0, v38, s[0:1]
	v_cndmask_b32_e64 v11, 0, v39, s[0:1]
	v_cndmask_b32_e64 v12, 0, v40, s[0:1]
	v_cndmask_b32_e64 v13, 0, v41, s[0:1]
	global_load_dwordx4 v[50:53], v[0:1], off offset:16
	global_load_dwordx4 v[46:49], v[0:1], off
	global_load_dwordx4 v[42:45], v[0:1], off offset:144
	global_load_dwordx4 v[38:41], v[0:1], off offset:128
	v_lshl_add_u32 v2, v220, 4, s14
	v_lshl_or_b32 v55, v207, 1, v2
	v_or_b32_e32 v2, s13, v220
	v_ashrrev_i32_e32 v3, 31, v2
	v_lshlrev_b32_e32 v0, 7, v109
	v_mov_b32_e32 v109, v201
	v_lshlrev_b64 v[2:3], 21, v[2:3]
	v_or3_b32 v104, v0, v103, s21
	v_lshl_add_u64 v[0:1], s[4:5], 0, v[108:109]
	s_cselect_b64 s[4:5], -1, 0
	v_lshl_add_u64 v[2:3], s[6:7], 0, v[2:3]
	s_ashr_i32 s3, s2, 31
	v_lshl_add_u64 v[2:3], s[2:3], 2, v[2:3]
	v_lshlrev_b32_e32 v4, 2, v208
	v_mov_b32_e32 v5, v201
	v_lshl_add_u64 v[96:97], v[2:3], 0, v[4:5]
	v_lshl_add_u32 v2, v214, 10, v54
	v_ashrrev_i32_e32 v3, 31, v2
	v_lshl_add_u64 v[2:3], v[2:3], 2, s[6:7]
	s_mov_b64 s[2:3], 0x8000000
	v_lshl_add_u64 v[98:99], v[2:3], 0, s[2:3]
	s_mov_b64 s[2:3], 0x8040000
	v_lshl_add_u64 v[100:101], v[2:3], 0, s[2:3]
	s_lshl_b32 s2, s19, 14
	s_lshl_b32 s3, s18, 9
	s_add_i32 s2, s2, s3
	v_mbcnt_lo_u32_b32 v2, -1, 0
	v_add_u32_e32 v106, s2, v55
	v_mbcnt_hi_u32_b32 v2, -1, v2
	v_mov_b64_e32 v[54:55], v[200:201]
	v_mov_b64_e32 v[58:59], v[200:201]
	v_cndmask_b32_e64 v14, 0, v14, s[0:1]
	v_cndmask_b32_e64 v15, 0, v15, s[0:1]
	v_cndmask_b32_e64 v16, 0, v16, s[0:1]
	v_cndmask_b32_e64 v17, 0, v17, s[0:1]
	v_cndmask_b32_e64 v18, 0, v18, s[0:1]
	v_cndmask_b32_e64 v19, 0, v19, s[0:1]
	v_cndmask_b32_e64 v20, 0, v20, s[0:1]
	v_cndmask_b32_e64 v21, 0, v21, s[0:1]
	v_cndmask_b32_e64 v22, 0, v22, s[0:1]
	v_cndmask_b32_e64 v23, 0, v23, s[0:1]
	v_cndmask_b32_e64 v24, 0, v24, s[0:1]
	v_cndmask_b32_e64 v25, 0, v25, s[0:1]
	v_cndmask_b32_e64 v26, 0, v26, s[0:1]
	v_cndmask_b32_e64 v27, 0, v27, s[0:1]
	v_cndmask_b32_e64 v28, 0, v28, s[0:1]
	v_cndmask_b32_e64 v29, 0, v29, s[0:1]
	v_cndmask_b32_e64 v30, 0, v30, s[0:1]
	v_cndmask_b32_e64 v31, 0, v31, s[0:1]
	v_cndmask_b32_e64 v32, 0, v32, s[0:1]
	v_cndmask_b32_e64 v33, 0, v33, s[0:1]
	v_cndmask_b32_e64 v34, 0, v34, s[0:1]
	v_cndmask_b32_e64 v35, 0, v35, s[0:1]
	v_cndmask_b32_e64 v36, 0, v36, s[0:1]
	v_cndmask_b32_e64 v37, 0, v37, s[0:1]
	v_lshlrev_b32_e32 v105, 9, v207
	s_mov_b64 s[6:7], 0
	s_mov_b32 s18, 0x40004000
	v_lshl_or_b32 v107, v2, 2, 32
	v_mov_b32_e32 v108, 0
	v_mov_b64_e32 v[56:57], v[202:203]
	v_mov_b64_e32 v[60:61], v[202:203]
	s_mov_b32 s24, 0
	v_lshl_add_u32 v166, s19, 14, v104
	v_mov_b32_e32 v177, 0
	s_not_b64 s[56:57], s[0:1]
	s_mov_b32 s37, 0x4038aa3b
	s_mov_b32 s38, 0xbfb8aa3b
	v_lshlrev_b32_e32 v222, 4, v198
	ds_read_b128 v[130:133], v222
	ds_read_b128 v[126:129], v222 offset:1024
	ds_read_b128 v[122:125], v222 offset:2048
	ds_read_b128 v[118:121], v222 offset:3072
	ds_read_b128 v[114:117], v222 offset:4096
	ds_read_b128 v[110:113], v222 offset:5120
	ds_read_b128 v[194:197], v222 offset:6144
	ds_read_b128 v[202:205], v222 offset:7168
	ds_read_b128 v[162:165], v222 offset:8192
	ds_read_b128 v[158:161], v222 offset:9216
	ds_read_b128 v[154:157], v222 offset:10240
	ds_read_b128 v[150:153], v222 offset:11264
	ds_read_b128 v[146:149], v222 offset:12288
	ds_read_b128 v[142:145], v222 offset:13312
	ds_read_b128 v[138:141], v222 offset:14336
	ds_read_b128 v[134:137], v222 offset:15360
	s_waitcnt vmcnt(0)
	v_mul_f32_e32 v185, 0xbfb8aa3b, v185
	v_mul_f32_e32 v186, 0xbfb8aa3b, v186
	v_mul_f32_e32 v187, 0x4038aa3b, v187
	v_mul_f32_e32 v188, 0xbfb8aa3b, v188
	v_cvt_pk_f16_f32 v180, v46, v47
	v_cvt_pk_f16_f32 v181, v48, v49
	v_cvt_pk_f16_f32 v182, v50, v51
	v_cvt_pk_f16_f32 v183, v52, v53
	v_cvt_pk_f16_f32 v218, v38, v39
	v_cvt_pk_f16_f32 v219, v40, v41
	v_cvt_pk_f16_f32 v220, v42, v43
	v_cvt_pk_f16_f32 v221, v44, v45
	s_mov_b32 s25, 1
	v_bitop3_b32 v2, s25, v193, 1 bitop3:0x6c
	v_add_u32_e32 v2, s25, v2
	v_min_i32_e32 v2, 0x1ff, v2
	s_and_b32 s12, s25, 1
	v_lshlrev_b32_e32 v200, 11, v2
	v_lshl_add_u64 v[2:3], v[210:211], 0, v[200:201]
	s_lshl_b32 s14, s12, 8
	v_lshl_add_u64 v[4:5], v[2:3], 0, s[14:15]
	global_load_dwordx4 v[46:49], v[4:5], off
	global_load_dwordx4 v[50:53], v[4:5], off offset:16
	global_load_dwordx4 v[38:41], v[4:5], off offset:128
	global_load_dwordx4 v[42:45], v[4:5], off offset:144
.Lstep_top:
	s_and_b32 s16, s24, 1
	s_cmp_eq_u32 s16, 0
	s_cselect_b64 s[2:3], s[0:1], s[56:57]
	s_xor_b32 s33, s16, 1
	s_lshl_b32 s28, s33, 17
	s_add_i32 s25, s24, 1
	s_add_i32 s27, s24, 2
	s_mov_b32 s17, 0
	s_cmp_eq_u32 s24, 0
	s_cbranch_scc1 .Lpoll_issued
	s_mov_b64 exec, s[2:3]
	buffer_load_dwordx4 v[62:65], v166, s[8:11], s28 offen sc1
	buffer_load_dwordx4 v[66:69], v166, s[8:11], s28 offen offset:512 sc1
	buffer_load_dwordx4 v[70:73], v166, s[8:11], s28 offen offset:1024 sc1
	buffer_load_dwordx4 v[74:77], v166, s[8:11], s28 offen offset:1536 sc1
	buffer_load_dwordx4 v[78:81], v166, s[8:11], s28 offen offset:2048 sc1
	buffer_load_dwordx4 v[82:85], v166, s[8:11], s28 offen offset:2560 sc1
	buffer_load_dwordx4 v[86:89], v166, s[8:11], s28 offen offset:3072 sc1
	buffer_load_dwordx4 v[90:93], v166, s[8:11], s28 offen offset:3584 sc1
	s_mov_b64 exec, -1
.Lpoll_issued:
	s_waitcnt lgkmcnt(0)
	v_mfma_f32_16x16x32_f16 v[6:9], v[130:133], v[180:183], v[6:9]
	s_add_i32 s12, s24, -1
	s_bfe_i32 s13, s12, 0x10001
	v_mfma_f32_16x16x32_f16 v[10:13], v[126:129], v[180:183], v[10:13]
	s_and_b32 s30, s13, 0x40004000
	v_mov_b32_e32 v3, 0xbfffbfff
	v_mfma_f32_16x16x32_f16 v[14:17], v[122:125], v[180:183], v[14:17]
	v_cndmask_b32_e64 v167, 0, v3, s[2:3]
	s_lshl_b32 s34, s24, 13
	v_mfma_f32_16x16x32_f16 v[18:21], v[118:121], v[180:183], v[18:21]
	s_and_b32 s34, s34, 0x4000
	s_lshl_b32 s14, s24, 10
	v_mfma_f32_16x16x32_f16 v[22:25], v[114:117], v[180:183], v[22:25]
	v_lshl_add_u64 v[178:179], s[14:15], 2, v[96:97]
	v_bitop3_b32 v2, s27, v193, 1 bitop3:0x6c
	v_mfma_f32_16x16x32_f16 v[26:29], v[110:113], v[180:183], v[26:29]
	v_add_u32_e32 v2, s27, v2
	v_min_i32_e32 v2, 0x1ff, v2
	v_mfma_f32_16x16x32_f16 v[30:33], v[194:197], v[180:183], v[30:33]
	s_and_b32 s12, s27, 1
	v_lshlrev_b32_e32 v200, 11, v2
	v_mfma_f32_16x16x32_f16 v[34:37], v[202:205], v[180:183], v[34:37]
	v_lshl_add_u64 v[2:3], v[210:211], 0, v[200:201]
	s_lshl_b32 s14, s12, 8
	s_waitcnt lgkmcnt(0)
	v_mfma_f32_16x16x32_f16 v[6:9], v[162:165], v[218:221], v[6:9]
	v_lshl_add_u64 v[4:5], v[2:3], 0, s[14:15]
	s_lshl_b32 s35, s16, 14
	v_mfma_f32_16x16x32_f16 v[10:13], v[158:161], v[218:221], v[10:13]
	s_bitset1_b32 s35, 17
	s_add_i32 s26, s35, s21
	v_mfma_f32_16x16x32_f16 v[14:17], v[154:157], v[218:221], v[14:17]
	v_lshlrev_b32_e32 v2, 4, v217
	v_add3_u32 v174, s26, v2, v103
	v_mfma_f32_16x16x32_f16 v[18:21], v[150:153], v[218:221], v[18:21]
	s_lshl_b32 s12, s20, 4
	s_add_i32 s12, s12, s35
	v_mfma_f32_16x16x32_f16 v[22:25], v[146:149], v[218:221], v[22:25]
	v_add3_u32 v175, s12, v105, v103
	v_lshl_add_u32 v176, s16, 17, v106
	v_mfma_f32_16x16x32_f16 v[26:29], v[142:145], v[218:221], v[26:29]
	s_and_b32 s31, s24, 15
	s_and_b32 s12, s24, 0x1f0
	v_mfma_f32_16x16x32_f16 v[30:33], v[138:141], v[218:221], v[30:33]
	s_add_i32 s12, s23, s12
	s_min_i32 s12, s12, 0x1ff
	v_mfma_f32_16x16x32_f16 v[34:37], v[134:137], v[218:221], v[34:37]
	s_ashr_i32 s13, s12, 31
	s_lshl_b64 s[12:13], s[12:13], 11
	v_lshl_add_u64 v[172:173], v[0:1], 0, s[12:13]
	s_cmp_eq_u32 s24, 0
	s_cbranch_scc1 .Lfirst_step
	s_waitcnt vmcnt(7)
	v_bitop3_b32 v168, v62, v63, s30 bitop3:0x7e
	v_bitop3_b32 v169, v64, v65, s30 bitop3:0x7e
	v_bitop3_b32 v168, v168, v169, s18 bitop3:0xa8
	v_cmp_ne_u32_e32 vcc, 0, v168
	s_and_b64 vcc, vcc, s[2:3]
	s_cbranch_vccnz .Lrestart0
	v_and_b32_e32 v62, v62, v167
	v_and_b32_e32 v63, v63, v167
	v_and_b32_e32 v64, v64, v167
	v_and_b32_e32 v65, v65, v167
	s_nop 1
.Lfast0:
	v_mfma_f32_16x16x32_f16 v[6:9], a[0:3], v[62:65], v[6:9]
	v_cvt_pk_f16_f32 v180, v46, v47
	v_cvt_pk_f16_f32 v181, v48, v49
	v_mfma_f32_16x16x32_f16 v[10:13], a[32:35], v[62:65], v[10:13]
	v_cvt_pk_f16_f32 v182, v50, v51
	v_cvt_pk_f16_f32 v183, v52, v53
	v_mfma_f32_16x16x32_f16 v[14:17], a[64:67], v[62:65], v[14:17]
	v_cvt_pk_f16_f32 v218, v38, v39
	v_cvt_pk_f16_f32 v219, v40, v41
	s_waitcnt vmcnt(6)
	v_mfma_f32_16x16x32_f16 v[18:21], a[96:99], v[62:65], v[18:21]
	v_bitop3_b32 v168, v66, v67, s30 bitop3:0x7e
	v_bitop3_b32 v169, v68, v69, s30 bitop3:0x7e
	v_mfma_f32_16x16x32_f16 v[22:25], a[128:131], v[62:65], v[22:25]
	v_bitop3_b32 v168, v168, v169, s18 bitop3:0xa8
	v_cmp_ne_u32_e32 vcc, 0, v168
	v_mfma_f32_16x16x32_f16 v[26:29], a[160:163], v[62:65], v[26:29]
	v_and_b32_e32 v66, v66, v167
	v_and_b32_e32 v67, v67, v167
	v_mfma_f32_16x16x32_f16 v[30:33], a[192:195], v[62:65], v[30:33]
	v_and_b32_e32 v68, v68, v167
	v_and_b32_e32 v69, v69, v167
	v_mfma_f32_16x16x32_f16 v[34:37], a[224:227], v[62:65], v[34:37]
	v_cvt_pk_f16_f32 v220, v42, v43
	v_cvt_pk_f16_f32 v221, v44, v45
	s_and_b64 vcc, vcc, s[2:3]
	s_cbranch_vccnz .Lrestart1
.Lfast1:
	v_mfma_f32_16x16x32_f16 v[6:9], a[4:7], v[66:69], v[6:9]
	v_xor_b32_e32 v222, 0x4000, v222
	ds_read_b128 v[130:133], v222
	v_mfma_f32_16x16x32_f16 v[10:13], a[36:39], v[66:69], v[10:13]
	ds_read_b128 v[126:129], v222 offset:1024
	ds_read_b128 v[122:125], v222 offset:2048
	v_mfma_f32_16x16x32_f16 v[14:17], a[68:71], v[66:69], v[14:17]
	s_waitcnt vmcnt(5)
	v_mfma_f32_16x16x32_f16 v[18:21], a[100:103], v[66:69], v[18:21]
	v_bitop3_b32 v168, v70, v71, s30 bitop3:0x7e
	v_bitop3_b32 v169, v72, v73, s30 bitop3:0x7e
	v_mfma_f32_16x16x32_f16 v[22:25], a[132:135], v[66:69], v[22:25]
	v_bitop3_b32 v168, v168, v169, s18 bitop3:0xa8
	v_cmp_ne_u32_e32 vcc, 0, v168
	v_mfma_f32_16x16x32_f16 v[26:29], a[164:167], v[66:69], v[26:29]
	v_and_b32_e32 v70, v70, v167
	v_and_b32_e32 v71, v71, v167
	v_mfma_f32_16x16x32_f16 v[30:33], a[196:199], v[66:69], v[30:33]
	v_and_b32_e32 v72, v72, v167
	v_and_b32_e32 v73, v73, v167
	v_mfma_f32_16x16x32_f16 v[34:37], a[228:231], v[66:69], v[34:37]
	s_and_b64 vcc, vcc, s[2:3]
	s_cbranch_vccnz .Lrestart2
.Lfast2:
	v_mfma_f32_16x16x32_f16 v[6:9], a[8:11], v[70:73], v[6:9]
	ds_read_b128 v[118:121], v222 offset:3072
	ds_read_b128 v[114:117], v222 offset:4096
	v_mfma_f32_16x16x32_f16 v[10:13], a[40:43], v[70:73], v[10:13]
	ds_read_b128 v[110:113], v222 offset:5120
	ds_read_b128 v[194:197], v222 offset:6144
	v_mfma_f32_16x16x32_f16 v[14:17], a[72:75], v[70:73], v[14:17]
	s_waitcnt vmcnt(4)
	v_mfma_f32_16x16x32_f16 v[18:21], a[104:107], v[70:73], v[18:21]
	v_bitop3_b32 v168, v74, v75, s30 bitop3:0x7e
	v_bitop3_b32 v169, v76, v77, s30 bitop3:0x7e
	v_mfma_f32_16x16x32_f16 v[22:25], a[136:139], v[70:73], v[22:25]
	v_bitop3_b32 v168, v168, v169, s18 bitop3:0xa8
	v_cmp_ne_u32_e32 vcc, 0, v168
	v_mfma_f32_16x16x32_f16 v[26:29], a[168:171], v[70:73], v[26:29]
	v_and_b32_e32 v74, v74, v167
	v_and_b32_e32 v75, v75, v167
	v_mfma_f32_16x16x32_f16 v[30:33], a[200:203], v[70:73], v[30:33]
	v_and_b32_e32 v76, v76, v167
	v_and_b32_e32 v77, v77, v167
	v_mfma_f32_16x16x32_f16 v[34:37], a[232:235], v[70:73], v[34:37]
	s_and_b64 vcc, vcc, s[2:3]
	s_cbranch_vccnz .Lrestart3
.Lfast3:
	v_mfma_f32_16x16x32_f16 v[6:9], a[12:15], v[74:77], v[6:9]
	ds_read_b128 v[202:205], v222 offset:7168
	ds_read_b128 v[162:165], v222 offset:8192
	v_mfma_f32_16x16x32_f16 v[10:13], a[44:47], v[74:77], v[10:13]
	ds_read_b128 v[158:161], v222 offset:9216
	ds_read_b128 v[154:157], v222 offset:10240
	v_mfma_f32_16x16x32_f16 v[14:17], a[76:79], v[74:77], v[14:17]
	s_waitcnt vmcnt(3)
	v_mfma_f32_16x16x32_f16 v[18:21], a[108:111], v[74:77], v[18:21]
	v_bitop3_b32 v168, v78, v79, s30 bitop3:0x7e
	v_bitop3_b32 v169, v80, v81, s30 bitop3:0x7e
	v_mfma_f32_16x16x32_f16 v[22:25], a[140:143], v[74:77], v[22:25]
	v_bitop3_b32 v168, v168, v169, s18 bitop3:0xa8
	v_cmp_ne_u32_e32 vcc, 0, v168
	v_mfma_f32_16x16x32_f16 v[26:29], a[172:175], v[74:77], v[26:29]
	v_and_b32_e32 v78, v78, v167
	v_and_b32_e32 v79, v79, v167
	v_mfma_f32_16x16x32_f16 v[30:33], a[204:207], v[74:77], v[30:33]
	v_and_b32_e32 v80, v80, v167
	v_and_b32_e32 v81, v81, v167
	v_mfma_f32_16x16x32_f16 v[34:37], a[236:239], v[74:77], v[34:37]
	s_and_b64 vcc, vcc, s[2:3]
	s_cbranch_vccnz .Lrestart4
.Lfast4:
	v_mfma_f32_16x16x32_f16 v[6:9], a[16:19], v[78:81], v[6:9]
	ds_read_b128 v[150:153], v222 offset:11264
	ds_read_b128 v[146:149], v222 offset:12288
	v_mfma_f32_16x16x32_f16 v[10:13], a[48:51], v[78:81], v[10:13]
	ds_read_b128 v[142:145], v222 offset:13312
	ds_read_b128 v[138:141], v222 offset:14336
	v_mfma_f32_16x16x32_f16 v[14:17], a[80:83], v[78:81], v[14:17]
	s_waitcnt vmcnt(2)
	v_mfma_f32_16x16x32_f16 v[18:21], a[112:115], v[78:81], v[18:21]
	v_bitop3_b32 v168, v82, v83, s30 bitop3:0x7e
	v_bitop3_b32 v169, v84, v85, s30 bitop3:0x7e
	v_mfma_f32_16x16x32_f16 v[22:25], a[144:147], v[78:81], v[22:25]
	v_bitop3_b32 v168, v168, v169, s18 bitop3:0xa8
	v_cmp_ne_u32_e32 vcc, 0, v168
	v_mfma_f32_16x16x32_f16 v[26:29], a[176:179], v[78:81], v[26:29]
	v_and_b32_e32 v82, v82, v167
	v_and_b32_e32 v83, v83, v167
	v_mfma_f32_16x16x32_f16 v[30:33], a[208:211], v[78:81], v[30:33]
	v_and_b32_e32 v84, v84, v167
	v_and_b32_e32 v85, v85, v167
	v_mfma_f32_16x16x32_f16 v[34:37], a[240:243], v[78:81], v[34:37]
	s_and_b64 vcc, vcc, s[2:3]
	s_cbranch_vccnz .Lrestart5
.Lfast5:
	v_mfma_f32_16x16x32_f16 v[6:9], a[20:23], v[82:85], v[6:9]
	ds_read_b128 v[134:137], v222 offset:15360
	v_mfma_f32_16x16x32_f16 v[10:13], a[52:55], v[82:85], v[10:13]
	v_mfma_f32_16x16x32_f16 v[14:17], a[84:87], v[82:85], v[14:17]
	s_waitcnt vmcnt(1)
	v_mfma_f32_16x16x32_f16 v[18:21], a[116:119], v[82:85], v[18:21]
	v_bitop3_b32 v168, v86, v87, s30 bitop3:0x7e
	v_bitop3_b32 v169, v88, v89, s30 bitop3:0x7e
	v_mfma_f32_16x16x32_f16 v[22:25], a[148:151], v[82:85], v[22:25]
	v_bitop3_b32 v168, v168, v169, s18 bitop3:0xa8
	v_cmp_ne_u32_e32 vcc, 0, v168
	v_mfma_f32_16x16x32_f16 v[26:29], a[180:183], v[82:85], v[26:29]
	v_and_b32_e32 v86, v86, v167
	v_and_b32_e32 v87, v87, v167
	v_mfma_f32_16x16x32_f16 v[30:33], a[212:215], v[82:85], v[30:33]
	v_and_b32_e32 v88, v88, v167
	v_and_b32_e32 v89, v89, v167
	v_mfma_f32_16x16x32_f16 v[34:37], a[244:247], v[82:85], v[34:37]
	s_and_b64 vcc, vcc, s[2:3]
	s_cbranch_vccnz .Lrestart6
.Lfast6:
	v_mfma_f32_16x16x32_f16 v[6:9], a[24:27], v[86:89], v[6:9]
	v_mfma_f32_16x16x32_f16 v[10:13], a[56:59], v[86:89], v[10:13]
	v_mfma_f32_16x16x32_f16 v[14:17], a[88:91], v[86:89], v[14:17]
	s_waitcnt vmcnt(0)
	v_mfma_f32_16x16x32_f16 v[18:21], a[120:123], v[86:89], v[18:21]
	v_bitop3_b32 v168, v90, v91, s30 bitop3:0x7e
	v_bitop3_b32 v169, v92, v93, s30 bitop3:0x7e
	v_mfma_f32_16x16x32_f16 v[22:25], a[152:155], v[86:89], v[22:25]
	v_bitop3_b32 v168, v168, v169, s18 bitop3:0xa8
	v_cmp_ne_u32_e32 vcc, 0, v168
	v_mfma_f32_16x16x32_f16 v[26:29], a[184:187], v[86:89], v[26:29]
	v_and_b32_e32 v90, v90, v167
	v_and_b32_e32 v91, v91, v167
	v_mfma_f32_16x16x32_f16 v[30:33], a[216:219], v[86:89], v[30:33]
	v_and_b32_e32 v92, v92, v167
	v_and_b32_e32 v93, v93, v167
	v_mfma_f32_16x16x32_f16 v[34:37], a[248:251], v[86:89], v[34:37]
	s_and_b64 vcc, vcc, s[2:3]
	s_cbranch_vccnz .Lrestart7

.Lrestart0:
	s_and_b64 vcc, exec, s[6:7]
	s_cbranch_vccnz .Lfast0
	s_add_i32 s17, s17, 1
	s_cmp_gt_u32 s17, 0x10000
	s_cselect_b64 s[6:7], -1, 0
	s_mov_b64 exec, s[2:3]
	buffer_load_dwordx4 v[62:65], v166, s[8:11], s28 offen sc1
	buffer_load_dwordx4 v[66:69], v166, s[8:11], s28 offen offset:512 sc1
	buffer_load_dwordx4 v[70:73], v166, s[8:11], s28 offen offset:1024 sc1
	buffer_load_dwordx4 v[74:77], v166, s[8:11], s28 offen offset:1536 sc1
	buffer_load_dwordx4 v[78:81], v166, s[8:11], s28 offen offset:2048 sc1
	buffer_load_dwordx4 v[82:85], v166, s[8:11], s28 offen offset:2560 sc1
	buffer_load_dwordx4 v[86:89], v166, s[8:11], s28 offen offset:3072 sc1
	buffer_load_dwordx4 v[90:93], v166, s[8:11], s28 offen offset:3584 sc1
	s_mov_b64 exec, -1
	s_waitcnt vmcnt(7)
	v_bitop3_b32 v168, v62, v63, s30 bitop3:0x7e
	v_bitop3_b32 v169, v64, v65, s30 bitop3:0x7e
	v_bitop3_b32 v168, v168, v169, s18 bitop3:0xa8
	v_cmp_ne_u32_e32 vcc, 0, v168
	s_and_b64 vcc, vcc, s[2:3]
	s_cbranch_vccnz .Lrestart0
	v_and_b32_e32 v62, v62, v167
	v_and_b32_e32 v63, v63, v167
	v_and_b32_e32 v64, v64, v167
	v_and_b32_e32 v65, v65, v167
	s_nop 1
	s_branch .Lfast0
.Lrestart1:
	s_and_b64 vcc, exec, s[6:7]
	s_cbranch_vccnz .Lfast1
	s_add_i32 s17, s17, 1
	s_cmp_gt_u32 s17, 0x10000
	s_cselect_b64 s[6:7], -1, 0
	s_mov_b64 exec, s[2:3]
	buffer_load_dwordx4 v[66:69], v166, s[8:11], s28 offen offset:512 sc1
	buffer_load_dwordx4 v[70:73], v166, s[8:11], s28 offen offset:1024 sc1
	buffer_load_dwordx4 v[74:77], v166, s[8:11], s28 offen offset:1536 sc1
	buffer_load_dwordx4 v[78:81], v166, s[8:11], s28 offen offset:2048 sc1
	buffer_load_dwordx4 v[82:85], v166, s[8:11], s28 offen offset:2560 sc1
	buffer_load_dwordx4 v[86:89], v166, s[8:11], s28 offen offset:3072 sc1
	buffer_load_dwordx4 v[90:93], v166, s[8:11], s28 offen offset:3584 sc1
	s_mov_b64 exec, -1
	s_waitcnt vmcnt(6)
	v_bitop3_b32 v168, v66, v67, s30 bitop3:0x7e
	v_bitop3_b32 v169, v68, v69, s30 bitop3:0x7e
	v_bitop3_b32 v168, v168, v169, s18 bitop3:0xa8
	v_cmp_ne_u32_e32 vcc, 0, v168
	s_and_b64 vcc, vcc, s[2:3]
	s_cbranch_vccnz .Lrestart1
	v_and_b32_e32 v66, v66, v167
	v_and_b32_e32 v67, v67, v167
	v_and_b32_e32 v68, v68, v167
	v_and_b32_e32 v69, v69, v167
	s_nop 1
	s_branch .Lfast1
.Lrestart2:
	s_and_b64 vcc, exec, s[6:7]
	s_cbranch_vccnz .Lfast2
	s_add_i32 s17, s17, 1
	s_cmp_gt_u32 s17, 0x10000
	s_cselect_b64 s[6:7], -1, 0
	s_mov_b64 exec, s[2:3]
	buffer_load_dwordx4 v[70:73], v166, s[8:11], s28 offen offset:1024 sc1
	buffer_load_dwordx4 v[74:77], v166, s[8:11], s28 offen offset:1536 sc1
	buffer_load_dwordx4 v[78:81], v166, s[8:11], s28 offen offset:2048 sc1
	buffer_load_dwordx4 v[82:85], v166, s[8:11], s28 offen offset:2560 sc1
	buffer_load_dwordx4 v[86:89], v166, s[8:11], s28 offen offset:3072 sc1
	buffer_load_dwordx4 v[90:93], v166, s[8:11], s28 offen offset:3584 sc1
	s_mov_b64 exec, -1
	s_waitcnt vmcnt(5)
	v_bitop3_b32 v168, v70, v71, s30 bitop3:0x7e
	v_bitop3_b32 v169, v72, v73, s30 bitop3:0x7e
	v_bitop3_b32 v168, v168, v169, s18 bitop3:0xa8
	v_cmp_ne_u32_e32 vcc, 0, v168
	s_and_b64 vcc, vcc, s[2:3]
	s_cbranch_vccnz .Lrestart2
	v_and_b32_e32 v70, v70, v167
	v_and_b32_e32 v71, v71, v167
	v_and_b32_e32 v72, v72, v167
	v_and_b32_e32 v73, v73, v167
	s_nop 1
	s_branch .Lfast2
.Lrestart3:
	s_and_b64 vcc, exec, s[6:7]
	s_cbranch_vccnz .Lfast3
	s_add_i32 s17, s17, 1
	s_cmp_gt_u32 s17, 0x10000
	s_cselect_b64 s[6:7], -1, 0
	s_mov_b64 exec, s[2:3]
	buffer_load_dwordx4 v[74:77], v166, s[8:11], s28 offen offset:1536 sc1
	buffer_load_dwordx4 v[78:81], v166, s[8:11], s28 offen offset:2048 sc1
	buffer_load_dwordx4 v[82:85], v166, s[8:11], s28 offen offset:2560 sc1
	buffer_load_dwordx4 v[86:89], v166, s[8:11], s28 offen offset:3072 sc1
	buffer_load_dwordx4 v[90:93], v166, s[8:11], s28 offen offset:3584 sc1
	s_mov_b64 exec, -1
	s_waitcnt vmcnt(4)
	v_bitop3_b32 v168, v74, v75, s30 bitop3:0x7e
	v_bitop3_b32 v169, v76, v77, s30 bitop3:0x7e
	v_bitop3_b32 v168, v168, v169, s18 bitop3:0xa8
	v_cmp_ne_u32_e32 vcc, 0, v168
	s_and_b64 vcc, vcc, s[2:3]
	s_cbranch_vccnz .Lrestart3
	v_and_b32_e32 v74, v74, v167
	v_and_b32_e32 v75, v75, v167
	v_and_b32_e32 v76, v76, v167
	v_and_b32_e32 v77, v77, v167
	s_nop 1
	s_branch .Lfast3
.Lrestart4:
	s_and_b64 vcc, exec, s[6:7]
	s_cbranch_vccnz .Lfast4
	s_add_i32 s17, s17, 1
	s_cmp_gt_u32 s17, 0x10000
	s_cselect_b64 s[6:7], -1, 0
	s_mov_b64 exec, s[2:3]
	buffer_load_dwordx4 v[78:81], v166, s[8:11], s28 offen offset:2048 sc1
	buffer_load_dwordx4 v[82:85], v166, s[8:11], s28 offen offset:2560 sc1
	buffer_load_dwordx4 v[86:89], v166, s[8:11], s28 offen offset:3072 sc1
	buffer_load_dwordx4 v[90:93], v166, s[8:11], s28 offen offset:3584 sc1
	s_mov_b64 exec, -1
	s_waitcnt vmcnt(3)
	v_bitop3_b32 v168, v78, v79, s30 bitop3:0x7e
	v_bitop3_b32 v169, v80, v81, s30 bitop3:0x7e
	v_bitop3_b32 v168, v168, v169, s18 bitop3:0xa8
	v_cmp_ne_u32_e32 vcc, 0, v168
	s_and_b64 vcc, vcc, s[2:3]
	s_cbranch_vccnz .Lrestart4
	v_and_b32_e32 v78, v78, v167
	v_and_b32_e32 v79, v79, v167
	v_and_b32_e32 v80, v80, v167
	v_and_b32_e32 v81, v81, v167
	s_nop 1
	s_branch .Lfast4
.Lrestart5:
	s_and_b64 vcc, exec, s[6:7]
	s_cbranch_vccnz .Lfast5
	s_add_i32 s17, s17, 1
	s_cmp_gt_u32 s17, 0x10000
	s_cselect_b64 s[6:7], -1, 0
	s_mov_b64 exec, s[2:3]
	buffer_load_dwordx4 v[82:85], v166, s[8:11], s28 offen offset:2560 sc1
	buffer_load_dwordx4 v[86:89], v166, s[8:11], s28 offen offset:3072 sc1
	buffer_load_dwordx4 v[90:93], v166, s[8:11], s28 offen offset:3584 sc1
	s_mov_b64 exec, -1
	s_waitcnt vmcnt(2)
	v_bitop3_b32 v168, v82, v83, s30 bitop3:0x7e
	v_bitop3_b32 v169, v84, v85, s30 bitop3:0x7e
	v_bitop3_b32 v168, v168, v169, s18 bitop3:0xa8
	v_cmp_ne_u32_e32 vcc, 0, v168
	s_and_b64 vcc, vcc, s[2:3]
	s_cbranch_vccnz .Lrestart5
	v_and_b32_e32 v82, v82, v167
	v_and_b32_e32 v83, v83, v167
	v_and_b32_e32 v84, v84, v167
	v_and_b32_e32 v85, v85, v167
	s_nop 1
	s_branch .Lfast5
.Lrestart6:
	s_and_b64 vcc, exec, s[6:7]
	s_cbranch_vccnz .Lfast6
	s_add_i32 s17, s17, 1
	s_cmp_gt_u32 s17, 0x10000
	s_cselect_b64 s[6:7], -1, 0
	s_mov_b64 exec, s[2:3]
	buffer_load_dwordx4 v[86:89], v166, s[8:11], s28 offen offset:3072 sc1
	buffer_load_dwordx4 v[90:93], v166, s[8:11], s28 offen offset:3584 sc1
	s_mov_b64 exec, -1
	s_waitcnt vmcnt(1)
	v_bitop3_b32 v168, v86, v87, s30 bitop3:0x7e
	v_bitop3_b32 v169, v88, v89, s30 bitop3:0x7e
	v_bitop3_b32 v168, v168, v169, s18 bitop3:0xa8
	v_cmp_ne_u32_e32 vcc, 0, v168
	s_and_b64 vcc, vcc, s[2:3]
	s_cbranch_vccnz .Lrestart6
	v_and_b32_e32 v86, v86, v167
	v_and_b32_e32 v87, v87, v167
	v_and_b32_e32 v88, v88, v167
	v_and_b32_e32 v89, v89, v167
	s_nop 1
	s_branch .Lfast6
.Lrestart7:
	s_and_b64 vcc, exec, s[6:7]
	s_cbranch_vccnz .Lfast7
	s_add_i32 s17, s17, 1
	s_cmp_gt_u32 s17, 0x10000
	s_cselect_b64 s[6:7], -1, 0
	s_mov_b64 exec, s[2:3]
	buffer_load_dwordx4 v[90:93], v166, s[8:11], s28 offen offset:3584 sc1
	s_mov_b64 exec, -1
	s_waitcnt vmcnt(0)
	v_bitop3_b32 v168, v90, v91, s30 bitop3:0x7e
	v_bitop3_b32 v169, v92, v93, s30 bitop3:0x7e
	v_bitop3_b32 v168, v168, v169, s18 bitop3:0xa8
	v_cmp_ne_u32_e32 vcc, 0, v168
	s_and_b64 vcc, vcc, s[2:3]
	s_cbranch_vccnz .Lrestart7
	v_and_b32_e32 v90, v90, v167
	v_and_b32_e32 v91, v91, v167
	v_and_b32_e32 v92, v92, v167
	v_and_b32_e32 v93, v93, v167
	s_nop 1
	s_branch .Lfast7
